# GEMM K-loops: LDS-DMA requests issued from the compute segment between the wave's own MFMAs (saddr form), waits vmcnt(6)/(2); plus P2 pipeline and epilogue hoists
# baseline (speedup 1.0000x reference)
.LBB0_178:
	ds_read_b128 v[148:151], v155
	ds_read_b128 v[160:163], v155 offset:1024
	ds_read_b128 v[164:167], v155 offset:2048
	ds_read_b128 v[168:171], v155 offset:3072
	ds_read_b128 v[172:175], v156
	ds_read_b128 v[176:179], v156 offset:1024
	ds_read_b128 v[180:183], v156 offset:2048
	ds_read_b128 v[184:187], v156 offset:3072
	s_add_u32 s26, s24, 0xfff80080
	s_addc_u32 s27, s25, -1
	s_cmp_eq_u32 s58, 28
	s_cselect_b32 s29, s17, s27
	s_cselect_b32 s28, s54, s26
	s_cselect_b32 s27, s15, s57
	s_cselect_b32 s26, s55, s56
	s_add_i32 m0, s23, 0xc000
	ds_read_b128 v[188:191], v157
	ds_read_b128 v[192:195], v157 offset:1024
	ds_read_b128 v[196:199], v157 offset:2048
	ds_read_b128 v[200:203], v157 offset:3072
	ds_read_b128 v[204:207], v157 offset:4096
	ds_read_b128 v[208:211], v157 offset:5120
	ds_read_b128 v[212:215], v157 offset:6144
	ds_read_b128 v[216:219], v157 offset:7168
	s_waitcnt vmcnt(6)
	s_waitcnt lgkmcnt(0)
	s_barrier
	s_setprio 1
	s_waitcnt lgkmcnt(0)
	v_mfma_f32_16x16x32_bf16 v[126:129], v[148:151], v[188:191], v[126:129]
	global_load_lds_dwordx4 v138, s[24:25]
	v_mfma_f32_16x16x32_bf16 v[122:125], v[164:167], v[188:191], v[122:125]
	s_add_i32 m0, s23, 0xe000
	v_mfma_f32_16x16x32_bf16 v[118:121], v[148:151], v[196:199], v[118:121]
	s_nop 0
	v_mfma_f32_16x16x32_bf16 v[110:113], v[164:167], v[196:199], v[110:113]
	global_load_lds_dwordx4 v140, s[24:25]
	v_mfma_f32_16x16x32_bf16 v[102:105], v[148:151], v[204:207], v[102:105]
	v_mfma_f32_16x16x32_bf16 v[94:97], v[164:167], v[204:207], v[94:97]
	v_mfma_f32_16x16x32_bf16 v[86:89], v[148:151], v[212:215], v[86:89]
	v_mfma_f32_16x16x32_bf16 v[78:81], v[164:167], v[212:215], v[78:81]
	v_mfma_f32_16x16x32_bf16 v[126:129], v[160:163], v[192:195], v[126:129]
	v_mfma_f32_16x16x32_bf16 v[122:125], v[168:171], v[192:195], v[122:125]
	v_mfma_f32_16x16x32_bf16 v[118:121], v[160:163], v[200:203], v[118:121]
	v_mfma_f32_16x16x32_bf16 v[110:113], v[168:171], v[200:203], v[110:113]
	v_mfma_f32_16x16x32_bf16 v[102:105], v[160:163], v[208:211], v[102:105]
	v_mfma_f32_16x16x32_bf16 v[94:97], v[168:171], v[208:211], v[94:97]
	v_mfma_f32_16x16x32_bf16 v[86:89], v[160:163], v[216:219], v[86:89]
	v_mfma_f32_16x16x32_bf16 v[78:81], v[168:171], v[216:219], v[78:81]
	s_setprio 0
	s_setprio 1
	v_mfma_f32_16x16x32_bf16 v[114:117], v[172:175], v[188:191], v[114:117]
	v_mfma_f32_16x16x32_bf16 v[106:109], v[180:183], v[188:191], v[106:109]
	v_mfma_f32_16x16x32_bf16 v[98:101], v[172:175], v[196:199], v[98:101]
	v_mfma_f32_16x16x32_bf16 v[90:93], v[180:183], v[196:199], v[90:93]
	v_mfma_f32_16x16x32_bf16 v[82:85], v[172:175], v[204:207], v[82:85]
	v_mfma_f32_16x16x32_bf16 v[74:77], v[180:183], v[204:207], v[74:77]
	v_mfma_f32_16x16x32_bf16 v[70:73], v[172:175], v[212:215], v[70:73]
	v_mfma_f32_16x16x32_bf16 v[66:69], v[180:183], v[212:215], v[66:69]
	v_mfma_f32_16x16x32_bf16 v[114:117], v[176:179], v[192:195], v[114:117]
	v_mfma_f32_16x16x32_bf16 v[106:109], v[184:187], v[192:195], v[106:109]
	v_mfma_f32_16x16x32_bf16 v[98:101], v[176:179], v[200:203], v[98:101]
	v_mfma_f32_16x16x32_bf16 v[90:93], v[184:187], v[200:203], v[90:93]
	v_mfma_f32_16x16x32_bf16 v[82:85], v[176:179], v[208:211], v[82:85]
	v_mfma_f32_16x16x32_bf16 v[74:77], v[184:187], v[208:211], v[74:77]
	v_mfma_f32_16x16x32_bf16 v[70:73], v[176:179], v[216:219], v[70:73]
	v_mfma_f32_16x16x32_bf16 v[66:69], v[184:187], v[216:219], v[66:69]
	s_setprio 0
	s_barrier
	s_add_i32 s59, s42, s31
	s_add_u32 s90, s26, s10
	s_addc_u32 s91, s27, s11
	s_mov_b32 m0, s59
	ds_read_b128 v[188:191], v157 offset:16384
	ds_read_b128 v[192:195], v157 offset:17408
	ds_read_b128 v[196:199], v157 offset:18432
	ds_read_b128 v[200:203], v157 offset:19456
	ds_read_b128 v[204:207], v157 offset:20480
	ds_read_b128 v[208:211], v157 offset:21504
	ds_read_b128 v[212:215], v157 offset:22528
	ds_read_b128 v[216:219], v157 offset:23552
	s_waitcnt vmcnt(2)
	s_waitcnt lgkmcnt(0)
	s_barrier
	s_setprio 1
	s_waitcnt lgkmcnt(0)
	v_mfma_f32_16x16x32_bf16 v[62:65], v[148:151], v[188:191], v[62:65]
	global_load_lds_dwordx4 v134, s[26:27]
	v_mfma_f32_16x16x32_bf16 v[58:61], v[164:167], v[188:191], v[58:61]
	s_add_i32 m0, s59, 0x2000
	v_mfma_f32_16x16x32_bf16 v[54:57], v[148:151], v[196:199], v[54:57]
	s_add_u32 s60, s26, 0x80000
	v_mfma_f32_16x16x32_bf16 v[46:49], v[164:167], v[196:199], v[46:49]
	s_addc_u32 s61, s27, 0
	v_mfma_f32_16x16x32_bf16 v[38:41], v[148:151], v[204:207], v[38:41]
	s_add_i32 s59, s43, s31
	v_mfma_f32_16x16x32_bf16 v[30:33], v[164:167], v[204:207], v[30:33]
	global_load_lds_dwordx4 v130, s[26:27]
	v_mfma_f32_16x16x32_bf16 v[22:25], v[148:151], v[212:215], v[22:25]
	s_mov_b32 m0, s59
	v_mfma_f32_16x16x32_bf16 v[14:17], v[164:167], v[212:215], v[14:17]
	s_nop 0
	v_mfma_f32_16x16x32_bf16 v[62:65], v[160:163], v[192:195], v[62:65]
	global_load_lds_dwordx4 v134, s[60:61]
	v_mfma_f32_16x16x32_bf16 v[58:61], v[168:171], v[192:195], v[58:61]
	s_add_i32 m0, s59, 0x2000
	v_mfma_f32_16x16x32_bf16 v[54:57], v[160:163], v[200:203], v[54:57]
	s_nop 0
	v_mfma_f32_16x16x32_bf16 v[46:49], v[168:171], v[200:203], v[46:49]
	global_load_lds_dwordx4 v130, s[60:61]
	v_mfma_f32_16x16x32_bf16 v[38:41], v[160:163], v[208:211], v[38:41]
	s_add_u32 s92, s28, s10
	v_mfma_f32_16x16x32_bf16 v[30:33], v[168:171], v[208:211], v[30:33]
	s_addc_u32 s93, s29, s11
	v_mfma_f32_16x16x32_bf16 v[22:25], v[160:163], v[216:219], v[22:25]
	s_mov_b32 m0, s23
	v_mfma_f32_16x16x32_bf16 v[14:17], v[168:171], v[216:219], v[14:17]
	s_nop 0
	s_setprio 0
	s_setprio 1
	v_mfma_f32_16x16x32_bf16 v[50:53], v[172:175], v[188:191], v[50:53]
	global_load_lds_dwordx4 v136, s[28:29]
	v_mfma_f32_16x16x32_bf16 v[42:45], v[180:183], v[188:191], v[42:45]
	s_mov_b32 m0, s35
	v_mfma_f32_16x16x32_bf16 v[34:37], v[172:175], v[196:199], v[34:37]
	s_nop 0
	v_mfma_f32_16x16x32_bf16 v[26:29], v[180:183], v[196:199], v[26:29]
	global_load_lds_dwordx4 v132, s[28:29]
	v_mfma_f32_16x16x32_bf16 v[18:21], v[172:175], v[204:207], v[18:21]
	v_mfma_f32_16x16x32_bf16 v[10:13], v[180:183], v[204:207], v[10:13]
	v_mfma_f32_16x16x32_bf16 v[6:9], v[172:175], v[212:215], v[6:9]
	v_mfma_f32_16x16x32_bf16 v[2:5], v[180:183], v[212:215], v[2:5]
	v_mfma_f32_16x16x32_bf16 v[50:53], v[176:179], v[192:195], v[50:53]
	v_mfma_f32_16x16x32_bf16 v[42:45], v[184:187], v[192:195], v[42:45]
	v_mfma_f32_16x16x32_bf16 v[34:37], v[176:179], v[200:203], v[34:37]
	v_mfma_f32_16x16x32_bf16 v[26:29], v[184:187], v[200:203], v[26:29]
	v_mfma_f32_16x16x32_bf16 v[18:21], v[176:179], v[208:211], v[18:21]
	v_mfma_f32_16x16x32_bf16 v[10:13], v[184:187], v[208:211], v[10:13]
	v_mfma_f32_16x16x32_bf16 v[6:9], v[176:179], v[216:219], v[6:9]
	v_mfma_f32_16x16x32_bf16 v[2:5], v[184:187], v[216:219], v[2:5]
	s_setprio 0
	s_barrier
	s_add_i32 s59, 0, 0x18000
	v_add_u32_e32 v159, s59, v153
	s_add_i32 s60, 0, 0x1c000
	ds_read_b128 v[148:151], v159
	ds_read_b128 v[160:163], v159 offset:1024
	ds_read_b128 v[164:167], v159 offset:2048
	ds_read_b128 v[168:171], v159 offset:3072
	v_add_u32_e32 v159, s60, v153
	ds_read_b128 v[172:175], v159
	ds_read_b128 v[176:179], v159 offset:1024
	ds_read_b128 v[180:183], v159 offset:2048
	ds_read_b128 v[184:187], v159 offset:3072
	s_add_u32 s28, s28, 0x80000
	s_addc_u32 s29, s29, 0
	s_mov_b32 m0, s36
	ds_read_b128 v[188:191], v157 offset:32768
	ds_read_b128 v[192:195], v157 offset:33792
	ds_read_b128 v[196:199], v157 offset:34816
	ds_read_b128 v[200:203], v157 offset:35840
	ds_read_b128 v[204:207], v157 offset:36864
	ds_read_b128 v[208:211], v157 offset:37888
	ds_read_b128 v[212:215], v157 offset:38912
	ds_read_b128 v[216:219], v157 offset:39936
	s_waitcnt vmcnt(6)
	s_waitcnt lgkmcnt(0)
	s_barrier
	s_setprio 1
	s_waitcnt lgkmcnt(0)
	v_mfma_f32_16x16x32_bf16 v[126:129], v[148:151], v[188:191], v[126:129]
	global_load_lds_dwordx4 v136, s[28:29]
	v_mfma_f32_16x16x32_bf16 v[122:125], v[164:167], v[188:191], v[122:125]
	s_mov_b32 m0, s37
	v_mfma_f32_16x16x32_bf16 v[118:121], v[148:151], v[196:199], v[118:121]
	s_nop 0
	v_mfma_f32_16x16x32_bf16 v[110:113], v[164:167], v[196:199], v[110:113]
	global_load_lds_dwordx4 v132, s[28:29]
	v_mfma_f32_16x16x32_bf16 v[102:105], v[148:151], v[204:207], v[102:105]
	v_mfma_f32_16x16x32_bf16 v[94:97], v[164:167], v[204:207], v[94:97]
	v_mfma_f32_16x16x32_bf16 v[86:89], v[148:151], v[212:215], v[86:89]
	v_mfma_f32_16x16x32_bf16 v[78:81], v[164:167], v[212:215], v[78:81]
	v_mfma_f32_16x16x32_bf16 v[126:129], v[160:163], v[192:195], v[126:129]
	v_mfma_f32_16x16x32_bf16 v[122:125], v[168:171], v[192:195], v[122:125]
	v_mfma_f32_16x16x32_bf16 v[118:121], v[160:163], v[200:203], v[118:121]
	v_mfma_f32_16x16x32_bf16 v[110:113], v[168:171], v[200:203], v[110:113]
	v_mfma_f32_16x16x32_bf16 v[102:105], v[160:163], v[208:211], v[102:105]
	v_mfma_f32_16x16x32_bf16 v[94:97], v[168:171], v[208:211], v[94:97]
	v_mfma_f32_16x16x32_bf16 v[86:89], v[160:163], v[216:219], v[86:89]
	v_mfma_f32_16x16x32_bf16 v[78:81], v[168:171], v[216:219], v[78:81]
	s_setprio 0
	s_setprio 1
	v_mfma_f32_16x16x32_bf16 v[114:117], v[172:175], v[188:191], v[114:117]
	v_mfma_f32_16x16x32_bf16 v[106:109], v[180:183], v[188:191], v[106:109]
	v_mfma_f32_16x16x32_bf16 v[98:101], v[172:175], v[196:199], v[98:101]
	v_mfma_f32_16x16x32_bf16 v[90:93], v[180:183], v[196:199], v[90:93]
	v_mfma_f32_16x16x32_bf16 v[82:85], v[172:175], v[204:207], v[82:85]
	v_mfma_f32_16x16x32_bf16 v[74:77], v[180:183], v[204:207], v[74:77]
	v_mfma_f32_16x16x32_bf16 v[70:73], v[172:175], v[212:215], v[70:73]
	v_mfma_f32_16x16x32_bf16 v[66:69], v[180:183], v[212:215], v[66:69]
	v_mfma_f32_16x16x32_bf16 v[114:117], v[176:179], v[192:195], v[114:117]
	v_mfma_f32_16x16x32_bf16 v[106:109], v[184:187], v[192:195], v[106:109]
	v_mfma_f32_16x16x32_bf16 v[98:101], v[176:179], v[200:203], v[98:101]
	v_mfma_f32_16x16x32_bf16 v[90:93], v[184:187], v[200:203], v[90:93]
	v_mfma_f32_16x16x32_bf16 v[82:85], v[176:179], v[208:211], v[82:85]
	v_mfma_f32_16x16x32_bf16 v[74:77], v[184:187], v[208:211], v[74:77]
	v_mfma_f32_16x16x32_bf16 v[70:73], v[176:179], v[216:219], v[70:73]
	v_mfma_f32_16x16x32_bf16 v[66:69], v[184:187], v[216:219], v[66:69]
	s_setprio 0
	s_barrier
	s_add_i32 s28, s59, s31
	s_mov_b32 m0, s28
	ds_read_b128 v[188:191], v157 offset:49152
	ds_read_b128 v[192:195], v157 offset:50176
	ds_read_b128 v[196:199], v157 offset:51200
	ds_read_b128 v[200:203], v157 offset:52224
	ds_read_b128 v[204:207], v157 offset:53248
	ds_read_b128 v[208:211], v157 offset:54272
	ds_read_b128 v[212:215], v157 offset:55296
	ds_read_b128 v[216:219], v157 offset:56320
	s_waitcnt vmcnt(2)
	s_waitcnt lgkmcnt(0)
	s_barrier
	s_setprio 1
	s_waitcnt lgkmcnt(0)
	v_mfma_f32_16x16x32_bf16 v[62:65], v[148:151], v[188:191], v[62:65]
	global_load_lds_dwordx4 v134, s[90:91]
	v_mfma_f32_16x16x32_bf16 v[58:61], v[164:167], v[188:191], v[58:61]
	s_add_i32 m0, s28, 0x2000
	v_mfma_f32_16x16x32_bf16 v[54:57], v[148:151], v[196:199], v[54:57]
	s_add_u32 s26, s26, 0x80080
	v_mfma_f32_16x16x32_bf16 v[46:49], v[164:167], v[196:199], v[46:49]
	s_addc_u32 s27, s27, 0
	v_mfma_f32_16x16x32_bf16 v[38:41], v[148:151], v[204:207], v[38:41]
	s_add_i32 s28, s60, s31
	v_mfma_f32_16x16x32_bf16 v[30:33], v[164:167], v[204:207], v[30:33]
	global_load_lds_dwordx4 v130, s[90:91]
	v_mfma_f32_16x16x32_bf16 v[22:25], v[148:151], v[212:215], v[22:25]
	s_mov_b32 m0, s28
	v_mfma_f32_16x16x32_bf16 v[14:17], v[164:167], v[212:215], v[14:17]
	s_nop 0
	v_mfma_f32_16x16x32_bf16 v[62:65], v[160:163], v[192:195], v[62:65]
	global_load_lds_dwordx4 v134, s[26:27]
	v_mfma_f32_16x16x32_bf16 v[58:61], v[168:171], v[192:195], v[58:61]
	s_add_i32 m0, s28, 0x2000
	v_mfma_f32_16x16x32_bf16 v[54:57], v[160:163], v[200:203], v[54:57]
	s_nop 0
	v_mfma_f32_16x16x32_bf16 v[46:49], v[168:171], v[200:203], v[46:49]
	global_load_lds_dwordx4 v130, s[26:27]
	v_mfma_f32_16x16x32_bf16 v[38:41], v[160:163], v[208:211], v[38:41]
	s_mov_b32 m0, s39
	v_mfma_f32_16x16x32_bf16 v[30:33], v[168:171], v[208:211], v[30:33]
	s_nop 0
	v_mfma_f32_16x16x32_bf16 v[22:25], v[160:163], v[216:219], v[22:25]
	global_load_lds_dwordx4 v136, s[92:93]
	v_mfma_f32_16x16x32_bf16 v[14:17], v[168:171], v[216:219], v[14:17]
	s_mov_b32 m0, s40
	s_setprio 0
	s_setprio 1
	v_mfma_f32_16x16x32_bf16 v[50:53], v[172:175], v[188:191], v[50:53]
	s_nop 0
	v_mfma_f32_16x16x32_bf16 v[42:45], v[180:183], v[188:191], v[42:45]
	global_load_lds_dwordx4 v132, s[92:93]
	v_mfma_f32_16x16x32_bf16 v[34:37], v[172:175], v[196:199], v[34:37]
	v_mfma_f32_16x16x32_bf16 v[26:29], v[180:183], v[196:199], v[26:29]
	v_mfma_f32_16x16x32_bf16 v[18:21], v[172:175], v[204:207], v[18:21]
	v_mfma_f32_16x16x32_bf16 v[10:13], v[180:183], v[204:207], v[10:13]
	v_mfma_f32_16x16x32_bf16 v[6:9], v[172:175], v[212:215], v[6:9]
	v_mfma_f32_16x16x32_bf16 v[2:5], v[180:183], v[212:215], v[2:5]
	v_mfma_f32_16x16x32_bf16 v[50:53], v[176:179], v[192:195], v[50:53]
	v_mfma_f32_16x16x32_bf16 v[42:45], v[184:187], v[192:195], v[42:45]
	v_mfma_f32_16x16x32_bf16 v[34:37], v[176:179], v[200:203], v[34:37]
	v_mfma_f32_16x16x32_bf16 v[26:29], v[184:187], v[200:203], v[26:29]
	v_mfma_f32_16x16x32_bf16 v[18:21], v[176:179], v[208:211], v[18:21]
	v_mfma_f32_16x16x32_bf16 v[10:13], v[184:187], v[208:211], v[10:13]
	v_mfma_f32_16x16x32_bf16 v[6:9], v[176:179], v[216:219], v[6:9]
	v_mfma_f32_16x16x32_bf16 v[2:5], v[184:187], v[216:219], v[2:5]
	s_setprio 0
	s_barrier
	s_add_i32 s58, s58, 2
	s_add_u32 s24, s24, 0x100
	s_addc_u32 s25, s25, 0
	s_add_u32 s56, s56, 0x100
	s_addc_u32 s57, s57, 0
	s_cmp_gt_u32 s58, 29
	s_cbranch_scc0 .LBB0_178
	s_and_b64 vcc, exec, s[12:13]
	s_cbranch_vccz .LBB0_181
	s_barrier

.LBB0_384:
	ds_read_b128 v[148:151], v155
	ds_read_b128 v[160:163], v155 offset:1024
	ds_read_b128 v[164:167], v155 offset:2048
	ds_read_b128 v[168:171], v155 offset:3072
	ds_read_b128 v[172:175], v156
	ds_read_b128 v[176:179], v156 offset:1024
	ds_read_b128 v[180:183], v156 offset:2048
	ds_read_b128 v[184:187], v156 offset:3072
	s_add_u32 s30, s28, 0xfff80080
	s_addc_u32 s31, s29, -1
	s_cmp_eq_u32 s59, 28
	s_cselect_b32 s35, s19, s31
	s_cselect_b32 s34, s25, s30
	s_cselect_b32 s31, s17, s58
	s_cselect_b32 s30, s56, s57
	s_add_i32 m0, s27, 0xc000
	ds_read_b128 v[188:191], v157
	ds_read_b128 v[192:195], v157 offset:1024
	ds_read_b128 v[196:199], v157 offset:2048
	ds_read_b128 v[200:203], v157 offset:3072
	ds_read_b128 v[204:207], v157 offset:4096
	ds_read_b128 v[208:211], v157 offset:5120
	ds_read_b128 v[212:215], v157 offset:6144
	ds_read_b128 v[216:219], v157 offset:7168
	s_waitcnt vmcnt(6)
	s_waitcnt lgkmcnt(0)
	s_barrier
	s_setprio 1
	s_waitcnt lgkmcnt(0)
	v_mfma_f32_16x16x32_bf16 v[126:129], v[148:151], v[188:191], v[126:129]
	global_load_lds_dwordx4 v138, s[28:29]
	v_mfma_f32_16x16x32_bf16 v[122:125], v[164:167], v[188:191], v[122:125]
	s_add_i32 m0, s27, 0xe000
	v_mfma_f32_16x16x32_bf16 v[110:113], v[148:151], v[196:199], v[110:113]
	s_nop 0
	v_mfma_f32_16x16x32_bf16 v[106:109], v[164:167], v[196:199], v[106:109]
	global_load_lds_dwordx4 v140, s[28:29]
	v_mfma_f32_16x16x32_bf16 v[94:97], v[148:151], v[204:207], v[94:97]
	v_mfma_f32_16x16x32_bf16 v[90:93], v[164:167], v[204:207], v[90:93]
	v_mfma_f32_16x16x32_bf16 v[78:81], v[148:151], v[212:215], v[78:81]
	v_mfma_f32_16x16x32_bf16 v[74:77], v[164:167], v[212:215], v[74:77]
	v_mfma_f32_16x16x32_bf16 v[126:129], v[160:163], v[192:195], v[126:129]
	v_mfma_f32_16x16x32_bf16 v[122:125], v[168:171], v[192:195], v[122:125]
	v_mfma_f32_16x16x32_bf16 v[110:113], v[160:163], v[200:203], v[110:113]
	v_mfma_f32_16x16x32_bf16 v[106:109], v[168:171], v[200:203], v[106:109]
	v_mfma_f32_16x16x32_bf16 v[94:97], v[160:163], v[208:211], v[94:97]
	v_mfma_f32_16x16x32_bf16 v[90:93], v[168:171], v[208:211], v[90:93]
	v_mfma_f32_16x16x32_bf16 v[78:81], v[160:163], v[216:219], v[78:81]
	v_mfma_f32_16x16x32_bf16 v[74:77], v[168:171], v[216:219], v[74:77]
	s_setprio 0
	s_setprio 1
	v_mfma_f32_16x16x32_bf16 v[118:121], v[172:175], v[188:191], v[118:121]
	v_mfma_f32_16x16x32_bf16 v[114:117], v[180:183], v[188:191], v[114:117]
	v_mfma_f32_16x16x32_bf16 v[102:105], v[172:175], v[196:199], v[102:105]
	v_mfma_f32_16x16x32_bf16 v[98:101], v[180:183], v[196:199], v[98:101]
	v_mfma_f32_16x16x32_bf16 v[86:89], v[172:175], v[204:207], v[86:89]
	v_mfma_f32_16x16x32_bf16 v[82:85], v[180:183], v[204:207], v[82:85]
	v_mfma_f32_16x16x32_bf16 v[70:73], v[172:175], v[212:215], v[70:73]
	v_mfma_f32_16x16x32_bf16 v[66:69], v[180:183], v[212:215], v[66:69]
	v_mfma_f32_16x16x32_bf16 v[118:121], v[176:179], v[192:195], v[118:121]
	v_mfma_f32_16x16x32_bf16 v[114:117], v[184:187], v[192:195], v[114:117]
	v_mfma_f32_16x16x32_bf16 v[102:105], v[176:179], v[200:203], v[102:105]
	v_mfma_f32_16x16x32_bf16 v[98:101], v[184:187], v[200:203], v[98:101]
	v_mfma_f32_16x16x32_bf16 v[86:89], v[176:179], v[208:211], v[86:89]
	v_mfma_f32_16x16x32_bf16 v[82:85], v[184:187], v[208:211], v[82:85]
	v_mfma_f32_16x16x32_bf16 v[70:73], v[176:179], v[216:219], v[70:73]
	v_mfma_f32_16x16x32_bf16 v[66:69], v[184:187], v[216:219], v[66:69]
	s_setprio 0
	s_barrier
	s_add_i32 s60, s45, s36
	s_add_u32 s90, s30, s12
	s_addc_u32 s91, s31, s13
	s_mov_b32 m0, s60
	ds_read_b128 v[188:191], v157 offset:16384
	ds_read_b128 v[192:195], v157 offset:17408
	ds_read_b128 v[196:199], v157 offset:18432
	ds_read_b128 v[200:203], v157 offset:19456
	ds_read_b128 v[204:207], v157 offset:20480
	ds_read_b128 v[208:211], v157 offset:21504
	ds_read_b128 v[212:215], v157 offset:22528
	ds_read_b128 v[216:219], v157 offset:23552
	s_waitcnt vmcnt(2)
	s_waitcnt lgkmcnt(0)
	s_barrier
	s_setprio 1
	s_waitcnt lgkmcnt(0)
	v_mfma_f32_16x16x32_bf16 v[62:65], v[148:151], v[188:191], v[62:65]
	global_load_lds_dwordx4 v132, s[30:31]
	v_mfma_f32_16x16x32_bf16 v[58:61], v[164:167], v[188:191], v[58:61]
	s_add_i32 m0, s60, 0x2000
	v_mfma_f32_16x16x32_bf16 v[46:49], v[148:151], v[196:199], v[46:49]
	s_add_u32 s60, s30, 0x80000
	v_mfma_f32_16x16x32_bf16 v[42:45], v[164:167], v[196:199], v[42:45]
	s_addc_u32 s61, s31, 0
	v_mfma_f32_16x16x32_bf16 v[30:33], v[148:151], v[204:207], v[30:33]
	s_add_i32 s62, s54, s36
	v_mfma_f32_16x16x32_bf16 v[26:29], v[164:167], v[204:207], v[26:29]
	global_load_lds_dwordx4 v136, s[30:31]
	v_mfma_f32_16x16x32_bf16 v[14:17], v[148:151], v[212:215], v[14:17]
	s_mov_b32 m0, s62
	v_mfma_f32_16x16x32_bf16 v[10:13], v[164:167], v[212:215], v[10:13]
	s_nop 0
	v_mfma_f32_16x16x32_bf16 v[62:65], v[160:163], v[192:195], v[62:65]
	global_load_lds_dwordx4 v132, s[60:61]
	v_mfma_f32_16x16x32_bf16 v[58:61], v[168:171], v[192:195], v[58:61]
	s_add_i32 m0, s62, 0x2000
	v_mfma_f32_16x16x32_bf16 v[46:49], v[160:163], v[200:203], v[46:49]
	s_nop 0
	v_mfma_f32_16x16x32_bf16 v[42:45], v[168:171], v[200:203], v[42:45]
	global_load_lds_dwordx4 v136, s[60:61]
	v_mfma_f32_16x16x32_bf16 v[30:33], v[160:163], v[208:211], v[30:33]
	s_add_u32 s92, s34, s12
	v_mfma_f32_16x16x32_bf16 v[26:29], v[168:171], v[208:211], v[26:29]
	s_addc_u32 s93, s35, s13
	v_mfma_f32_16x16x32_bf16 v[14:17], v[160:163], v[216:219], v[14:17]
	s_mov_b32 m0, s27
	v_mfma_f32_16x16x32_bf16 v[10:13], v[168:171], v[216:219], v[10:13]
	s_nop 0
	s_setprio 0
	s_setprio 1
	v_mfma_f32_16x16x32_bf16 v[54:57], v[172:175], v[188:191], v[54:57]
	global_load_lds_dwordx4 v130, s[34:35]
	v_mfma_f32_16x16x32_bf16 v[50:53], v[180:183], v[188:191], v[50:53]
	s_mov_b32 m0, s37
	v_mfma_f32_16x16x32_bf16 v[38:41], v[172:175], v[196:199], v[38:41]
	s_nop 0
	v_mfma_f32_16x16x32_bf16 v[34:37], v[180:183], v[196:199], v[34:37]
	global_load_lds_dwordx4 v134, s[34:35]
	v_mfma_f32_16x16x32_bf16 v[22:25], v[172:175], v[204:207], v[22:25]
	v_mfma_f32_16x16x32_bf16 v[18:21], v[180:183], v[204:207], v[18:21]
	v_mfma_f32_16x16x32_bf16 v[6:9], v[172:175], v[212:215], v[6:9]
	v_mfma_f32_16x16x32_bf16 v[2:5], v[180:183], v[212:215], v[2:5]
	v_mfma_f32_16x16x32_bf16 v[54:57], v[176:179], v[192:195], v[54:57]
	v_mfma_f32_16x16x32_bf16 v[50:53], v[184:187], v[192:195], v[50:53]
	v_mfma_f32_16x16x32_bf16 v[38:41], v[176:179], v[200:203], v[38:41]
	v_mfma_f32_16x16x32_bf16 v[34:37], v[184:187], v[200:203], v[34:37]
	v_mfma_f32_16x16x32_bf16 v[22:25], v[176:179], v[208:211], v[22:25]
	v_mfma_f32_16x16x32_bf16 v[18:21], v[184:187], v[208:211], v[18:21]
	v_mfma_f32_16x16x32_bf16 v[6:9], v[176:179], v[216:219], v[6:9]
	v_mfma_f32_16x16x32_bf16 v[2:5], v[184:187], v[216:219], v[2:5]
	s_setprio 0
	s_barrier
	s_add_i32 s60, 0, 0x18000
	s_add_i32 s61, 0, 0x1c000
	v_add_u32_e32 v168, s60, v153
	v_add_u32_e32 v184, s61, v153
	ds_read_b128 v[148:151], v168
	ds_read_b128 v[160:163], v168 offset:1024
	ds_read_b128 v[164:167], v168 offset:2048
	ds_read_b128 v[168:171], v168 offset:3072
	ds_read_b128 v[172:175], v184
	ds_read_b128 v[176:179], v184 offset:1024
	ds_read_b128 v[180:183], v184 offset:2048
	ds_read_b128 v[184:187], v184 offset:3072
	s_add_u32 s34, s34, 0x80000
	s_addc_u32 s35, s35, 0
	s_mov_b32 m0, s38
	ds_read_b128 v[188:191], v157 offset:32768
	ds_read_b128 v[192:195], v157 offset:33792
	ds_read_b128 v[196:199], v157 offset:34816
	ds_read_b128 v[200:203], v157 offset:35840
	ds_read_b128 v[204:207], v157 offset:36864
	ds_read_b128 v[208:211], v157 offset:37888
	ds_read_b128 v[212:215], v157 offset:38912
	ds_read_b128 v[216:219], v157 offset:39936
	s_waitcnt vmcnt(6)
	s_waitcnt lgkmcnt(0)
	s_barrier
	s_setprio 1
	s_waitcnt lgkmcnt(0)
	v_mfma_f32_16x16x32_bf16 v[126:129], v[148:151], v[188:191], v[126:129]
	global_load_lds_dwordx4 v130, s[34:35]
	v_mfma_f32_16x16x32_bf16 v[122:125], v[164:167], v[188:191], v[122:125]
	s_mov_b32 m0, s39
	v_mfma_f32_16x16x32_bf16 v[110:113], v[148:151], v[196:199], v[110:113]
	s_nop 0
	v_mfma_f32_16x16x32_bf16 v[106:109], v[164:167], v[196:199], v[106:109]
	global_load_lds_dwordx4 v134, s[34:35]
	v_mfma_f32_16x16x32_bf16 v[94:97], v[148:151], v[204:207], v[94:97]
	v_mfma_f32_16x16x32_bf16 v[90:93], v[164:167], v[204:207], v[90:93]
	v_mfma_f32_16x16x32_bf16 v[78:81], v[148:151], v[212:215], v[78:81]
	v_mfma_f32_16x16x32_bf16 v[74:77], v[164:167], v[212:215], v[74:77]
	v_mfma_f32_16x16x32_bf16 v[126:129], v[160:163], v[192:195], v[126:129]
	v_mfma_f32_16x16x32_bf16 v[122:125], v[168:171], v[192:195], v[122:125]
	v_mfma_f32_16x16x32_bf16 v[110:113], v[160:163], v[200:203], v[110:113]
	v_mfma_f32_16x16x32_bf16 v[106:109], v[168:171], v[200:203], v[106:109]
	v_mfma_f32_16x16x32_bf16 v[94:97], v[160:163], v[208:211], v[94:97]
	v_mfma_f32_16x16x32_bf16 v[90:93], v[168:171], v[208:211], v[90:93]
	v_mfma_f32_16x16x32_bf16 v[78:81], v[160:163], v[216:219], v[78:81]
	v_mfma_f32_16x16x32_bf16 v[74:77], v[168:171], v[216:219], v[74:77]
	s_setprio 0
	s_setprio 1
	v_mfma_f32_16x16x32_bf16 v[118:121], v[172:175], v[188:191], v[118:121]
	v_mfma_f32_16x16x32_bf16 v[114:117], v[180:183], v[188:191], v[114:117]
	v_mfma_f32_16x16x32_bf16 v[102:105], v[172:175], v[196:199], v[102:105]
	v_mfma_f32_16x16x32_bf16 v[98:101], v[180:183], v[196:199], v[98:101]
	v_mfma_f32_16x16x32_bf16 v[86:89], v[172:175], v[204:207], v[86:89]
	v_mfma_f32_16x16x32_bf16 v[82:85], v[180:183], v[204:207], v[82:85]
	v_mfma_f32_16x16x32_bf16 v[70:73], v[172:175], v[212:215], v[70:73]
	v_mfma_f32_16x16x32_bf16 v[66:69], v[180:183], v[212:215], v[66:69]
	v_mfma_f32_16x16x32_bf16 v[118:121], v[176:179], v[192:195], v[118:121]
	v_mfma_f32_16x16x32_bf16 v[114:117], v[184:187], v[192:195], v[114:117]
	v_mfma_f32_16x16x32_bf16 v[102:105], v[176:179], v[200:203], v[102:105]
	v_mfma_f32_16x16x32_bf16 v[98:101], v[184:187], v[200:203], v[98:101]
	v_mfma_f32_16x16x32_bf16 v[86:89], v[176:179], v[208:211], v[86:89]
	v_mfma_f32_16x16x32_bf16 v[82:85], v[184:187], v[208:211], v[82:85]
	v_mfma_f32_16x16x32_bf16 v[70:73], v[176:179], v[216:219], v[70:73]
	v_mfma_f32_16x16x32_bf16 v[66:69], v[184:187], v[216:219], v[66:69]
	s_setprio 0
	s_barrier
	s_add_i32 s34, s60, s36
	s_mov_b32 m0, s34
	ds_read_b128 v[188:191], v157 offset:49152
	ds_read_b128 v[192:195], v157 offset:50176
	ds_read_b128 v[196:199], v157 offset:51200
	ds_read_b128 v[200:203], v157 offset:52224
	ds_read_b128 v[204:207], v157 offset:53248
	ds_read_b128 v[208:211], v157 offset:54272
	ds_read_b128 v[212:215], v157 offset:55296
	ds_read_b128 v[216:219], v157 offset:56320
	s_waitcnt vmcnt(2)
	s_waitcnt lgkmcnt(0)
	s_barrier
	s_setprio 1
	s_waitcnt lgkmcnt(0)
	v_mfma_f32_16x16x32_bf16 v[62:65], v[148:151], v[188:191], v[62:65]
	global_load_lds_dwordx4 v132, s[90:91]
	v_mfma_f32_16x16x32_bf16 v[58:61], v[164:167], v[188:191], v[58:61]
	s_add_i32 m0, s34, 0x2000
	v_mfma_f32_16x16x32_bf16 v[46:49], v[148:151], v[196:199], v[46:49]
	s_add_u32 s30, s30, 0x80080
	v_mfma_f32_16x16x32_bf16 v[42:45], v[164:167], v[196:199], v[42:45]
	s_addc_u32 s31, s31, 0
	v_mfma_f32_16x16x32_bf16 v[30:33], v[148:151], v[204:207], v[30:33]
	s_add_i32 s34, s61, s36
	v_mfma_f32_16x16x32_bf16 v[26:29], v[164:167], v[204:207], v[26:29]
	global_load_lds_dwordx4 v136, s[90:91]
	v_mfma_f32_16x16x32_bf16 v[14:17], v[148:151], v[212:215], v[14:17]
	s_mov_b32 m0, s34
	v_mfma_f32_16x16x32_bf16 v[10:13], v[164:167], v[212:215], v[10:13]
	s_nop 0
	v_mfma_f32_16x16x32_bf16 v[62:65], v[160:163], v[192:195], v[62:65]
	global_load_lds_dwordx4 v132, s[30:31]
	v_mfma_f32_16x16x32_bf16 v[58:61], v[168:171], v[192:195], v[58:61]
	s_add_i32 m0, s34, 0x2000
	v_mfma_f32_16x16x32_bf16 v[46:49], v[160:163], v[200:203], v[46:49]
	s_nop 0
	v_mfma_f32_16x16x32_bf16 v[42:45], v[168:171], v[200:203], v[42:45]
	global_load_lds_dwordx4 v136, s[30:31]
	v_mfma_f32_16x16x32_bf16 v[30:33], v[160:163], v[208:211], v[30:33]
	s_mov_b32 m0, s41
	v_mfma_f32_16x16x32_bf16 v[26:29], v[168:171], v[208:211], v[26:29]
	s_nop 0
	v_mfma_f32_16x16x32_bf16 v[14:17], v[160:163], v[216:219], v[14:17]
	global_load_lds_dwordx4 v130, s[92:93]
	v_mfma_f32_16x16x32_bf16 v[10:13], v[168:171], v[216:219], v[10:13]
	s_mov_b32 m0, s42
	s_setprio 0
	s_setprio 1
	v_mfma_f32_16x16x32_bf16 v[54:57], v[172:175], v[188:191], v[54:57]
	s_nop 0
	v_mfma_f32_16x16x32_bf16 v[50:53], v[180:183], v[188:191], v[50:53]
	global_load_lds_dwordx4 v134, s[92:93]
	v_mfma_f32_16x16x32_bf16 v[38:41], v[172:175], v[196:199], v[38:41]
	v_mfma_f32_16x16x32_bf16 v[34:37], v[180:183], v[196:199], v[34:37]
	v_mfma_f32_16x16x32_bf16 v[22:25], v[172:175], v[204:207], v[22:25]
	v_mfma_f32_16x16x32_bf16 v[18:21], v[180:183], v[204:207], v[18:21]
	v_mfma_f32_16x16x32_bf16 v[6:9], v[172:175], v[212:215], v[6:9]
	v_mfma_f32_16x16x32_bf16 v[2:5], v[180:183], v[212:215], v[2:5]
	v_mfma_f32_16x16x32_bf16 v[54:57], v[176:179], v[192:195], v[54:57]
	v_mfma_f32_16x16x32_bf16 v[50:53], v[184:187], v[192:195], v[50:53]
	v_mfma_f32_16x16x32_bf16 v[38:41], v[176:179], v[200:203], v[38:41]
	v_mfma_f32_16x16x32_bf16 v[34:37], v[184:187], v[200:203], v[34:37]
	v_mfma_f32_16x16x32_bf16 v[22:25], v[176:179], v[208:211], v[22:25]
	v_mfma_f32_16x16x32_bf16 v[18:21], v[184:187], v[208:211], v[18:21]
	v_mfma_f32_16x16x32_bf16 v[6:9], v[176:179], v[216:219], v[6:9]
	v_mfma_f32_16x16x32_bf16 v[2:5], v[184:187], v[216:219], v[2:5]
	s_setprio 0
	s_barrier
	s_add_i32 s59, s59, 2
	s_add_u32 s28, s28, 0x100
	s_addc_u32 s29, s29, 0
	s_add_u32 s57, s57, 0x100
	s_addc_u32 s58, s58, 0
	s_cmp_gt_u32 s59, 29
	s_cbranch_scc0 .LBB0_384
	s_and_b64 vcc, exec, s[14:15]
	s_cbranch_vccz .LBB0_387
	s_barrier

.LBB0_471:
	ds_read_b128 v[148:151], v160
	ds_read_b128 v[152:155], v160 offset:1024
	ds_read_b128 v[166:169], v160 offset:2048
	ds_read_b128 v[170:173], v160 offset:3072
	ds_read_b128 v[174:177], v161
	ds_read_b128 v[178:181], v161 offset:1024
	ds_read_b128 v[182:185], v161 offset:2048
	ds_read_b128 v[186:189], v161 offset:3072
	s_add_u32 s28, s26, 0xfff80080
	s_addc_u32 s29, s27, -1
	s_cmp_eq_u32 s59, 28
	s_cselect_b32 s31, s19, s29
	s_cselect_b32 s30, s55, s28
	s_cselect_b32 s29, s17, s58
	s_cselect_b32 s28, s56, s57
	s_add_i32 m0, s25, 0xc000
	ds_read_b128 v[190:193], v162
	ds_read_b128 v[194:197], v162 offset:1024
	ds_read_b128 v[198:201], v162 offset:2048
	ds_read_b128 v[202:205], v162 offset:3072
	ds_read_b128 v[206:209], v162 offset:4096
	ds_read_b128 v[210:213], v162 offset:5120
	ds_read_b128 v[214:217], v162 offset:6144
	ds_read_b128 v[218:221], v162 offset:7168
	s_waitcnt vmcnt(6)
	s_waitcnt lgkmcnt(0)
	s_barrier
	s_setprio 1
	s_waitcnt lgkmcnt(0)
	v_mfma_f32_16x16x32_bf16 v[118:121], v[148:151], v[190:193], v[118:121]
	global_load_lds_dwordx4 v138, s[26:27]
	v_mfma_f32_16x16x32_bf16 v[114:117], v[166:169], v[190:193], v[114:117]
	s_add_i32 m0, s25, 0xe000
	v_mfma_f32_16x16x32_bf16 v[102:105], v[148:151], v[198:201], v[102:105]
	s_nop 0
	v_mfma_f32_16x16x32_bf16 v[98:101], v[166:169], v[198:201], v[98:101]
	global_load_lds_dwordx4 v140, s[26:27]
	v_mfma_f32_16x16x32_bf16 v[86:89], v[148:151], v[206:209], v[86:89]
	v_mfma_f32_16x16x32_bf16 v[82:85], v[166:169], v[206:209], v[82:85]
	v_mfma_f32_16x16x32_bf16 v[74:77], v[148:151], v[214:217], v[74:77]
	v_mfma_f32_16x16x32_bf16 v[70:73], v[166:169], v[214:217], v[70:73]
	v_mfma_f32_16x16x32_bf16 v[118:121], v[152:155], v[194:197], v[118:121]
	v_mfma_f32_16x16x32_bf16 v[114:117], v[170:173], v[194:197], v[114:117]
	v_mfma_f32_16x16x32_bf16 v[102:105], v[152:155], v[202:205], v[102:105]
	v_mfma_f32_16x16x32_bf16 v[98:101], v[170:173], v[202:205], v[98:101]
	v_mfma_f32_16x16x32_bf16 v[86:89], v[152:155], v[210:213], v[86:89]
	v_mfma_f32_16x16x32_bf16 v[82:85], v[170:173], v[210:213], v[82:85]
	v_mfma_f32_16x16x32_bf16 v[74:77], v[152:155], v[218:221], v[74:77]
	v_mfma_f32_16x16x32_bf16 v[70:73], v[170:173], v[218:221], v[70:73]
	s_setprio 0
	s_setprio 1
	v_mfma_f32_16x16x32_bf16 v[126:129], v[174:177], v[190:193], v[126:129]
	v_mfma_f32_16x16x32_bf16 v[122:125], v[182:185], v[190:193], v[122:125]
	v_mfma_f32_16x16x32_bf16 v[110:113], v[174:177], v[198:201], v[110:113]
	v_mfma_f32_16x16x32_bf16 v[106:109], v[182:185], v[198:201], v[106:109]
	v_mfma_f32_16x16x32_bf16 v[94:97], v[174:177], v[206:209], v[94:97]
	v_mfma_f32_16x16x32_bf16 v[90:93], v[182:185], v[206:209], v[90:93]
	v_mfma_f32_16x16x32_bf16 v[78:81], v[174:177], v[214:217], v[78:81]
	v_mfma_f32_16x16x32_bf16 v[66:69], v[182:185], v[214:217], v[66:69]
	v_mfma_f32_16x16x32_bf16 v[126:129], v[178:181], v[194:197], v[126:129]
	v_mfma_f32_16x16x32_bf16 v[122:125], v[186:189], v[194:197], v[122:125]
	v_mfma_f32_16x16x32_bf16 v[110:113], v[178:181], v[202:205], v[110:113]
	v_mfma_f32_16x16x32_bf16 v[106:109], v[186:189], v[202:205], v[106:109]
	v_mfma_f32_16x16x32_bf16 v[94:97], v[178:181], v[210:213], v[94:97]
	v_mfma_f32_16x16x32_bf16 v[90:93], v[186:189], v[210:213], v[90:93]
	v_mfma_f32_16x16x32_bf16 v[78:81], v[178:181], v[218:221], v[78:81]
	v_mfma_f32_16x16x32_bf16 v[66:69], v[186:189], v[218:221], v[66:69]
	s_setprio 0
	s_barrier
	s_add_i32 s60, s44, s34
	s_add_u32 s90, s28, s12
	s_addc_u32 s91, s29, s13
	s_mov_b32 m0, s60
	ds_read_b128 v[190:193], v162 offset:16384
	ds_read_b128 v[194:197], v162 offset:17408
	ds_read_b128 v[198:201], v162 offset:18432
	ds_read_b128 v[202:205], v162 offset:19456
	ds_read_b128 v[206:209], v162 offset:20480
	ds_read_b128 v[210:213], v162 offset:21504
	ds_read_b128 v[214:217], v162 offset:22528
	ds_read_b128 v[218:221], v162 offset:23552
	s_waitcnt vmcnt(2)
	s_waitcnt lgkmcnt(0)
	s_barrier
	s_setprio 1
	s_waitcnt lgkmcnt(0)
	v_mfma_f32_16x16x32_bf16 v[58:61], v[148:151], v[190:193], v[58:61]
	global_load_lds_dwordx4 v134, s[28:29]
	v_mfma_f32_16x16x32_bf16 v[54:57], v[166:169], v[190:193], v[54:57]
	s_add_i32 m0, s60, 0x2000
	v_mfma_f32_16x16x32_bf16 v[42:45], v[148:151], v[198:201], v[42:45]
	s_add_u32 s60, s28, 0x80000
	v_mfma_f32_16x16x32_bf16 v[38:41], v[166:169], v[198:201], v[38:41]
	s_addc_u32 s61, s29, 0
	v_mfma_f32_16x16x32_bf16 v[26:29], v[148:151], v[206:209], v[26:29]
	s_add_i32 s62, s45, s34
	v_mfma_f32_16x16x32_bf16 v[22:25], v[166:169], v[206:209], v[22:25]
	global_load_lds_dwordx4 v130, s[28:29]
	v_mfma_f32_16x16x32_bf16 v[6:9], v[148:151], v[214:217], v[6:9]
	s_mov_b32 m0, s62
	v_mfma_f32_16x16x32_bf16 v[2:5], v[166:169], v[214:217], v[2:5]
	s_nop 0
	v_mfma_f32_16x16x32_bf16 v[58:61], v[152:155], v[194:197], v[58:61]
	global_load_lds_dwordx4 v134, s[60:61]
	v_mfma_f32_16x16x32_bf16 v[54:57], v[170:173], v[194:197], v[54:57]
	s_add_i32 m0, s62, 0x2000
	v_mfma_f32_16x16x32_bf16 v[42:45], v[152:155], v[202:205], v[42:45]
	s_nop 0
	v_mfma_f32_16x16x32_bf16 v[38:41], v[170:173], v[202:205], v[38:41]
	global_load_lds_dwordx4 v130, s[60:61]
	v_mfma_f32_16x16x32_bf16 v[26:29], v[152:155], v[210:213], v[26:29]
	s_add_u32 s92, s30, s12
	v_mfma_f32_16x16x32_bf16 v[22:25], v[170:173], v[210:213], v[22:25]
	s_addc_u32 s93, s31, s13
	v_mfma_f32_16x16x32_bf16 v[6:9], v[152:155], v[218:221], v[6:9]
	s_mov_b32 m0, s25
	v_mfma_f32_16x16x32_bf16 v[2:5], v[170:173], v[218:221], v[2:5]
	s_nop 0
	s_setprio 0
	s_setprio 1
	v_mfma_f32_16x16x32_bf16 v[62:65], v[174:177], v[190:193], v[62:65]
	global_load_lds_dwordx4 v136, s[30:31]
	v_mfma_f32_16x16x32_bf16 v[50:53], v[182:185], v[190:193], v[50:53]
	s_mov_b32 m0, s37
	v_mfma_f32_16x16x32_bf16 v[46:49], v[174:177], v[198:201], v[46:49]
	s_nop 0
	v_mfma_f32_16x16x32_bf16 v[34:37], v[182:185], v[198:201], v[34:37]
	global_load_lds_dwordx4 v132, s[30:31]
	v_mfma_f32_16x16x32_bf16 v[30:33], v[174:177], v[206:209], v[30:33]
	v_mfma_f32_16x16x32_bf16 v[18:21], v[182:185], v[206:209], v[18:21]
	v_mfma_f32_16x16x32_bf16 v[14:17], v[174:177], v[214:217], v[14:17]
	v_mfma_f32_16x16x32_bf16 v[10:13], v[182:185], v[214:217], v[10:13]
	v_mfma_f32_16x16x32_bf16 v[62:65], v[178:181], v[194:197], v[62:65]
	v_mfma_f32_16x16x32_bf16 v[50:53], v[186:189], v[194:197], v[50:53]
	v_mfma_f32_16x16x32_bf16 v[46:49], v[178:181], v[202:205], v[46:49]
	v_mfma_f32_16x16x32_bf16 v[34:37], v[186:189], v[202:205], v[34:37]
	v_mfma_f32_16x16x32_bf16 v[30:33], v[178:181], v[210:213], v[30:33]
	v_mfma_f32_16x16x32_bf16 v[18:21], v[186:189], v[210:213], v[18:21]
	v_mfma_f32_16x16x32_bf16 v[14:17], v[178:181], v[218:221], v[14:17]
	v_mfma_f32_16x16x32_bf16 v[10:13], v[186:189], v[218:221], v[10:13]
	s_setprio 0
	s_barrier
	s_add_i32 s60, 0, 0x18000
	v_add_u32_e32 v165, s60, v157
	s_add_i32 s61, 0, 0x1c000
	ds_read_b128 v[148:151], v165
	ds_read_b128 v[152:155], v165 offset:1024
	ds_read_b128 v[166:169], v165 offset:2048
	ds_read_b128 v[170:173], v165 offset:3072
	v_add_u32_e32 v165, s61, v157
	ds_read_b128 v[174:177], v165
	ds_read_b128 v[178:181], v165 offset:1024
	ds_read_b128 v[182:185], v165 offset:2048
	ds_read_b128 v[186:189], v165 offset:3072
	s_add_u32 s30, s30, 0x80000
	s_addc_u32 s31, s31, 0
	s_mov_b32 m0, s38
	ds_read_b128 v[190:193], v162 offset:32768
	ds_read_b128 v[194:197], v162 offset:33792
	ds_read_b128 v[198:201], v162 offset:34816
	ds_read_b128 v[202:205], v162 offset:35840
	ds_read_b128 v[206:209], v162 offset:36864
	ds_read_b128 v[210:213], v162 offset:37888
	ds_read_b128 v[214:217], v162 offset:38912
	ds_read_b128 v[218:221], v162 offset:39936
	s_waitcnt vmcnt(6)
	s_waitcnt lgkmcnt(0)
	s_barrier
	s_setprio 1
	s_waitcnt lgkmcnt(0)
	v_mfma_f32_16x16x32_bf16 v[118:121], v[148:151], v[190:193], v[118:121]
	global_load_lds_dwordx4 v136, s[30:31]
	v_mfma_f32_16x16x32_bf16 v[114:117], v[166:169], v[190:193], v[114:117]
	s_mov_b32 m0, s39
	v_mfma_f32_16x16x32_bf16 v[102:105], v[148:151], v[198:201], v[102:105]
	s_nop 0
	v_mfma_f32_16x16x32_bf16 v[98:101], v[166:169], v[198:201], v[98:101]
	global_load_lds_dwordx4 v132, s[30:31]
	v_mfma_f32_16x16x32_bf16 v[86:89], v[148:151], v[206:209], v[86:89]
	v_mfma_f32_16x16x32_bf16 v[82:85], v[166:169], v[206:209], v[82:85]
	v_mfma_f32_16x16x32_bf16 v[74:77], v[148:151], v[214:217], v[74:77]
	v_mfma_f32_16x16x32_bf16 v[70:73], v[166:169], v[214:217], v[70:73]
	v_mfma_f32_16x16x32_bf16 v[118:121], v[152:155], v[194:197], v[118:121]
	v_mfma_f32_16x16x32_bf16 v[114:117], v[170:173], v[194:197], v[114:117]
	v_mfma_f32_16x16x32_bf16 v[102:105], v[152:155], v[202:205], v[102:105]
	v_mfma_f32_16x16x32_bf16 v[98:101], v[170:173], v[202:205], v[98:101]
	v_mfma_f32_16x16x32_bf16 v[86:89], v[152:155], v[210:213], v[86:89]
	v_mfma_f32_16x16x32_bf16 v[82:85], v[170:173], v[210:213], v[82:85]
	v_mfma_f32_16x16x32_bf16 v[74:77], v[152:155], v[218:221], v[74:77]
	v_mfma_f32_16x16x32_bf16 v[70:73], v[170:173], v[218:221], v[70:73]
	s_setprio 0
	s_setprio 1
	v_mfma_f32_16x16x32_bf16 v[126:129], v[174:177], v[190:193], v[126:129]
	v_mfma_f32_16x16x32_bf16 v[122:125], v[182:185], v[190:193], v[122:125]
	v_mfma_f32_16x16x32_bf16 v[110:113], v[174:177], v[198:201], v[110:113]
	v_mfma_f32_16x16x32_bf16 v[106:109], v[182:185], v[198:201], v[106:109]
	v_mfma_f32_16x16x32_bf16 v[94:97], v[174:177], v[206:209], v[94:97]
	v_mfma_f32_16x16x32_bf16 v[90:93], v[182:185], v[206:209], v[90:93]
	v_mfma_f32_16x16x32_bf16 v[78:81], v[174:177], v[214:217], v[78:81]
	v_mfma_f32_16x16x32_bf16 v[66:69], v[182:185], v[214:217], v[66:69]
	v_mfma_f32_16x16x32_bf16 v[126:129], v[178:181], v[194:197], v[126:129]
	v_mfma_f32_16x16x32_bf16 v[122:125], v[186:189], v[194:197], v[122:125]
	v_mfma_f32_16x16x32_bf16 v[110:113], v[178:181], v[202:205], v[110:113]
	v_mfma_f32_16x16x32_bf16 v[106:109], v[186:189], v[202:205], v[106:109]
	v_mfma_f32_16x16x32_bf16 v[94:97], v[178:181], v[210:213], v[94:97]
	v_mfma_f32_16x16x32_bf16 v[90:93], v[186:189], v[210:213], v[90:93]
	v_mfma_f32_16x16x32_bf16 v[78:81], v[178:181], v[218:221], v[78:81]
	v_mfma_f32_16x16x32_bf16 v[66:69], v[186:189], v[218:221], v[66:69]
	s_setprio 0
	s_barrier
	s_add_i32 s30, s60, s34
	s_mov_b32 m0, s30
	ds_read_b128 v[190:193], v162 offset:49152
	ds_read_b128 v[194:197], v162 offset:50176
	ds_read_b128 v[198:201], v162 offset:51200
	ds_read_b128 v[202:205], v162 offset:52224
	ds_read_b128 v[206:209], v162 offset:53248
	ds_read_b128 v[210:213], v162 offset:54272
	ds_read_b128 v[214:217], v162 offset:55296
	ds_read_b128 v[218:221], v162 offset:56320
	s_waitcnt vmcnt(2)
	s_waitcnt lgkmcnt(0)
	s_barrier
	s_setprio 1
	s_waitcnt lgkmcnt(0)
	v_mfma_f32_16x16x32_bf16 v[58:61], v[148:151], v[190:193], v[58:61]
	global_load_lds_dwordx4 v134, s[90:91]
	v_mfma_f32_16x16x32_bf16 v[54:57], v[166:169], v[190:193], v[54:57]
	s_add_i32 m0, s30, 0x2000
	v_mfma_f32_16x16x32_bf16 v[42:45], v[148:151], v[198:201], v[42:45]
	s_add_u32 s28, s28, 0x80080
	v_mfma_f32_16x16x32_bf16 v[38:41], v[166:169], v[198:201], v[38:41]
	s_addc_u32 s29, s29, 0
	v_mfma_f32_16x16x32_bf16 v[26:29], v[148:151], v[206:209], v[26:29]
	s_add_i32 s30, s61, s34
	v_mfma_f32_16x16x32_bf16 v[22:25], v[166:169], v[206:209], v[22:25]
	global_load_lds_dwordx4 v130, s[90:91]
	v_mfma_f32_16x16x32_bf16 v[6:9], v[148:151], v[214:217], v[6:9]
	s_mov_b32 m0, s30
	v_mfma_f32_16x16x32_bf16 v[2:5], v[166:169], v[214:217], v[2:5]
	s_nop 0
	v_mfma_f32_16x16x32_bf16 v[58:61], v[152:155], v[194:197], v[58:61]
	global_load_lds_dwordx4 v134, s[28:29]
	v_mfma_f32_16x16x32_bf16 v[54:57], v[170:173], v[194:197], v[54:57]
	s_add_i32 m0, s30, 0x2000
	v_mfma_f32_16x16x32_bf16 v[42:45], v[152:155], v[202:205], v[42:45]
	s_nop 0
	v_mfma_f32_16x16x32_bf16 v[38:41], v[170:173], v[202:205], v[38:41]
	global_load_lds_dwordx4 v130, s[28:29]
	v_mfma_f32_16x16x32_bf16 v[26:29], v[152:155], v[210:213], v[26:29]
	s_mov_b32 m0, s41
	v_mfma_f32_16x16x32_bf16 v[22:25], v[170:173], v[210:213], v[22:25]
	s_nop 0
	v_mfma_f32_16x16x32_bf16 v[6:9], v[152:155], v[218:221], v[6:9]
	global_load_lds_dwordx4 v136, s[92:93]
	v_mfma_f32_16x16x32_bf16 v[2:5], v[170:173], v[218:221], v[2:5]
	s_mov_b32 m0, s42
	s_setprio 0
	s_setprio 1
	v_mfma_f32_16x16x32_bf16 v[62:65], v[174:177], v[190:193], v[62:65]
	s_nop 0
	v_mfma_f32_16x16x32_bf16 v[50:53], v[182:185], v[190:193], v[50:53]
	global_load_lds_dwordx4 v132, s[92:93]
	v_mfma_f32_16x16x32_bf16 v[46:49], v[174:177], v[198:201], v[46:49]
	v_mfma_f32_16x16x32_bf16 v[34:37], v[182:185], v[198:201], v[34:37]
	v_mfma_f32_16x16x32_bf16 v[30:33], v[174:177], v[206:209], v[30:33]
	v_mfma_f32_16x16x32_bf16 v[18:21], v[182:185], v[206:209], v[18:21]
	v_mfma_f32_16x16x32_bf16 v[14:17], v[174:177], v[214:217], v[14:17]
	v_mfma_f32_16x16x32_bf16 v[10:13], v[182:185], v[214:217], v[10:13]
	v_mfma_f32_16x16x32_bf16 v[62:65], v[178:181], v[194:197], v[62:65]
	v_mfma_f32_16x16x32_bf16 v[50:53], v[186:189], v[194:197], v[50:53]
	v_mfma_f32_16x16x32_bf16 v[46:49], v[178:181], v[202:205], v[46:49]
	v_mfma_f32_16x16x32_bf16 v[34:37], v[186:189], v[202:205], v[34:37]
	v_mfma_f32_16x16x32_bf16 v[30:33], v[178:181], v[210:213], v[30:33]
	v_mfma_f32_16x16x32_bf16 v[18:21], v[186:189], v[210:213], v[18:21]
	v_mfma_f32_16x16x32_bf16 v[14:17], v[178:181], v[218:221], v[14:17]
	v_mfma_f32_16x16x32_bf16 v[10:13], v[186:189], v[218:221], v[10:13]
	s_setprio 0
	s_barrier
	s_add_i32 s59, s59, 2
	s_add_u32 s26, s26, 0x100
	s_addc_u32 s27, s27, 0
	s_add_u32 s57, s57, 0x100
	s_addc_u32 s58, s58, 0
	s_cmp_gt_u32 s59, 29
	s_cbranch_scc0 .LBB0_471
	s_and_b64 vcc, exec, s[14:15]
	s_cbranch_vccz .LBB0_474
	s_barrier

.LBB0_556:
	ds_read_b128 v[162:165], v155
	ds_read_b128 v[166:169], v155 offset:1024
	ds_read_b128 v[170:173], v155 offset:2048
	ds_read_b128 v[174:177], v155 offset:3072
	ds_read_b128 v[178:181], v156
	ds_read_b128 v[182:185], v156 offset:1024
	ds_read_b128 v[224:227], v156 offset:2048
	ds_read_b128 v[228:231], v156 offset:3072
	s_add_u32 s22, s20, 0xfff50080
	s_addc_u32 s23, s21, -1
	s_cmp_eq_u32 s55, 40
	s_cselect_b32 s25, s1, s23
	s_cselect_b32 s24, s0, s22
	s_cselect_b32 s23, s19, s54
	s_cselect_b32 s22, s18, s49
	s_add_i32 m0, s30, 0xc000
	ds_read_b128 v[192:195], v157
	ds_read_b128 v[196:199], v157 offset:1024
	ds_read_b128 v[200:203], v157 offset:2048
	ds_read_b128 v[204:207], v157 offset:3072
	ds_read_b128 v[208:211], v157 offset:4096
	ds_read_b128 v[212:215], v157 offset:5120
	ds_read_b128 v[216:219], v157 offset:6144
	ds_read_b128 v[220:223], v157 offset:7168
	s_waitcnt vmcnt(6)
	s_waitcnt lgkmcnt(0)
	s_barrier
	s_setprio 1
	s_waitcnt lgkmcnt(0)
	s_nop 0
	v_mfma_scale_f32_16x16x128_f8f6f4 v[126:129], v[162:169], v[192:199], v[126:129], v160, v159 op_sel_hi:[0,0,0]
	global_load_lds_dwordx4 v138, s[20:21]
	v_mfma_scale_f32_16x16x128_f8f6f4 v[122:125], v[170:177], v[192:199], v[122:125], v160, v159 op_sel_hi:[0,0,0]
	s_add_i32 m0, s30, 0xe000
	v_mfma_scale_f32_16x16x128_f8f6f4 v[110:113], v[162:169], v[200:207], v[110:113], v160, v159 op_sel_hi:[0,0,0]
	s_nop 0
	v_mfma_scale_f32_16x16x128_f8f6f4 v[106:109], v[170:177], v[200:207], v[106:109], v160, v159 op_sel_hi:[0,0,0]
	global_load_lds_dwordx4 v140, s[20:21]
	v_mfma_scale_f32_16x16x128_f8f6f4 v[94:97], v[162:169], v[208:215], v[94:97], v160, v159 op_sel_hi:[0,0,0]
	v_mfma_scale_f32_16x16x128_f8f6f4 v[90:93], v[170:177], v[208:215], v[90:93], v160, v159 op_sel_hi:[0,0,0]
	v_mfma_scale_f32_16x16x128_f8f6f4 v[78:81], v[162:169], v[216:223], v[78:81], v160, v159 op_sel_hi:[0,0,0]
	v_mfma_scale_f32_16x16x128_f8f6f4 v[74:77], v[170:177], v[216:223], v[74:77], v160, v159 op_sel_hi:[0,0,0]
	s_setprio 0
	s_setprio 1
	s_nop 0
	v_mfma_scale_f32_16x16x128_f8f6f4 v[118:121], v[178:185], v[192:199], v[118:121], v160, v159 op_sel_hi:[0,0,0]
	v_mfma_scale_f32_16x16x128_f8f6f4 v[114:117], v[224:231], v[192:199], v[114:117], v160, v159 op_sel_hi:[0,0,0]
	v_mfma_scale_f32_16x16x128_f8f6f4 v[102:105], v[178:185], v[200:207], v[102:105], v160, v159 op_sel_hi:[0,0,0]
	v_mfma_scale_f32_16x16x128_f8f6f4 v[98:101], v[224:231], v[200:207], v[98:101], v160, v159 op_sel_hi:[0,0,0]
	v_mfma_scale_f32_16x16x128_f8f6f4 v[86:89], v[178:185], v[208:215], v[86:89], v160, v159 op_sel_hi:[0,0,0]
	v_mfma_scale_f32_16x16x128_f8f6f4 v[82:85], v[224:231], v[208:215], v[82:85], v160, v159 op_sel_hi:[0,0,0]
	v_mfma_scale_f32_16x16x128_f8f6f4 v[70:73], v[178:185], v[216:223], v[70:73], v160, v159 op_sel_hi:[0,0,0]
	v_mfma_scale_f32_16x16x128_f8f6f4 v[66:69], v[224:231], v[216:223], v[66:69], v160, v159 op_sel_hi:[0,0,0]
	s_setprio 0
	s_barrier
	s_add_i32 s56, s40, s29
	s_add_u32 s90, s22, s14
	s_addc_u32 s91, s23, s15
	s_mov_b32 m0, s56
	ds_read_b128 v[192:195], v157 offset:16384
	ds_read_b128 v[196:199], v157 offset:17408
	ds_read_b128 v[200:203], v157 offset:18432
	ds_read_b128 v[204:207], v157 offset:19456
	ds_read_b128 v[208:211], v157 offset:20480
	ds_read_b128 v[212:215], v157 offset:21504
	ds_read_b128 v[216:219], v157 offset:22528
	ds_read_b128 v[220:223], v157 offset:23552
	s_waitcnt vmcnt(2)
	s_waitcnt lgkmcnt(0)
	s_barrier
	s_setprio 1
	s_waitcnt lgkmcnt(0)
	s_nop 0
	v_mfma_scale_f32_16x16x128_f8f6f4 v[62:65], v[162:169], v[192:199], v[62:65], v160, v159 op_sel_hi:[0,0,0]
	global_load_lds_dwordx4 v132, s[22:23]
	s_add_i32 m0, s56, 0x2000
	v_mfma_scale_f32_16x16x128_f8f6f4 v[58:61], v[170:177], v[192:199], v[58:61], v160, v159 op_sel_hi:[0,0,0]
	s_add_u32 s56, s22, 0xb0000
	s_addc_u32 s57, s23, 0
	v_mfma_scale_f32_16x16x128_f8f6f4 v[46:49], v[162:169], v[200:207], v[46:49], v160, v159 op_sel_hi:[0,0,0]
	s_add_i32 s58, s41, s29
	global_load_lds_dwordx4 v136, s[22:23]
	v_mfma_scale_f32_16x16x128_f8f6f4 v[42:45], v[170:177], v[200:207], v[42:45], v160, v159 op_sel_hi:[0,0,0]
	s_mov_b32 m0, s58
	s_add_u32 s92, s24, s14
	v_mfma_scale_f32_16x16x128_f8f6f4 v[30:33], v[162:169], v[208:215], v[30:33], v160, v159 op_sel_hi:[0,0,0]
	s_addc_u32 s93, s25, s15
	s_nop 0
	v_mfma_scale_f32_16x16x128_f8f6f4 v[26:29], v[170:177], v[208:215], v[26:29], v160, v159 op_sel_hi:[0,0,0]
	global_load_lds_dwordx4 v132, s[56:57]
	s_add_i32 m0, s58, 0x2000
	v_mfma_scale_f32_16x16x128_f8f6f4 v[14:17], v[162:169], v[216:223], v[14:17], v160, v159 op_sel_hi:[0,0,0]
	s_nop 0
	global_load_lds_dwordx4 v136, s[56:57]
	v_mfma_scale_f32_16x16x128_f8f6f4 v[10:13], v[170:177], v[216:223], v[10:13], v160, v159 op_sel_hi:[0,0,0]
	s_mov_b32 m0, s30
	s_nop 0
	s_setprio 0
	s_setprio 1
	s_nop 0
	v_mfma_scale_f32_16x16x128_f8f6f4 v[54:57], v[178:185], v[192:199], v[54:57], v160, v159 op_sel_hi:[0,0,0]
	global_load_lds_dwordx4 v130, s[24:25]
	s_mov_b32 m0, s31
	v_mfma_scale_f32_16x16x128_f8f6f4 v[50:53], v[224:231], v[192:199], v[50:53], v160, v159 op_sel_hi:[0,0,0]
	s_nop 0
	global_load_lds_dwordx4 v134, s[24:25]
	v_mfma_scale_f32_16x16x128_f8f6f4 v[38:41], v[178:185], v[200:207], v[38:41], v160, v159 op_sel_hi:[0,0,0]
	v_mfma_scale_f32_16x16x128_f8f6f4 v[34:37], v[224:231], v[200:207], v[34:37], v160, v159 op_sel_hi:[0,0,0]
	v_mfma_scale_f32_16x16x128_f8f6f4 v[148:151], v[178:185], v[208:215], v[22:25], v160, v159 op_sel_hi:[0,0,0]
	v_mfma_scale_f32_16x16x128_f8f6f4 v[186:189], v[224:231], v[208:215], v[18:21], v160, v159 op_sel_hi:[0,0,0]
	v_mfma_scale_f32_16x16x128_f8f6f4 v[178:181], v[178:185], v[216:223], v[6:9], v160, v159 op_sel_hi:[0,0,0]
	v_mfma_scale_f32_16x16x128_f8f6f4 v[182:185], v[224:231], v[216:223], v[2:5], v160, v159 op_sel_hi:[0,0,0]
	s_setprio 0
	s_barrier
	s_add_i32 s56, 0, 0x18000
	s_add_i32 s57, 0, 0x1c000
	v_add_u32_e32 v22, s56, v153
	v_add_u32_e32 v174, s57, v153
	s_nop 0
	ds_read_b128 v[2:5], v22
	ds_read_b128 v[6:9], v22 offset:1024
	ds_read_b128 v[18:21], v22 offset:2048
	ds_read_b128 v[22:25], v22 offset:3072
	ds_read_b128 v[162:165], v174
	ds_read_b128 v[166:169], v174 offset:1024
	ds_read_b128 v[170:173], v174 offset:2048
	ds_read_b128 v[174:177], v174 offset:3072
	s_add_u32 s24, s24, 0xb0000
	s_addc_u32 s25, s25, 0
	s_mov_b32 m0, s33
	ds_read_b128 v[192:195], v157 offset:32768
	ds_read_b128 v[196:199], v157 offset:33792
	ds_read_b128 v[200:203], v157 offset:34816
	ds_read_b128 v[204:207], v157 offset:35840
	ds_read_b128 v[208:211], v157 offset:36864
	ds_read_b128 v[212:215], v157 offset:37888
	ds_read_b128 v[216:219], v157 offset:38912
	ds_read_b128 v[220:223], v157 offset:39936
	s_waitcnt vmcnt(6)
	s_waitcnt lgkmcnt(0)
	s_barrier
	s_setprio 1
	s_waitcnt lgkmcnt(0)
	s_nop 0
	v_mfma_scale_f32_16x16x128_f8f6f4 v[126:129], v[2:9], v[192:199], v[126:129], v160, v159 op_sel_hi:[0,0,0]
	global_load_lds_dwordx4 v130, s[24:25]
	v_mfma_scale_f32_16x16x128_f8f6f4 v[122:125], v[18:25], v[192:199], v[122:125], v160, v159 op_sel_hi:[0,0,0]
	s_mov_b32 m0, s34
	v_mfma_scale_f32_16x16x128_f8f6f4 v[110:113], v[2:9], v[200:207], v[110:113], v160, v159 op_sel_hi:[0,0,0]
	s_nop 0
	v_mfma_scale_f32_16x16x128_f8f6f4 v[106:109], v[18:25], v[200:207], v[106:109], v160, v159 op_sel_hi:[0,0,0]
	global_load_lds_dwordx4 v134, s[24:25]
	v_mfma_scale_f32_16x16x128_f8f6f4 v[94:97], v[2:9], v[208:215], v[94:97], v160, v159 op_sel_hi:[0,0,0]
	v_mfma_scale_f32_16x16x128_f8f6f4 v[90:93], v[18:25], v[208:215], v[90:93], v160, v159 op_sel_hi:[0,0,0]
	v_mfma_scale_f32_16x16x128_f8f6f4 v[78:81], v[2:9], v[216:223], v[78:81], v160, v159 op_sel_hi:[0,0,0]
	v_mfma_scale_f32_16x16x128_f8f6f4 v[74:77], v[18:25], v[216:223], v[74:77], v160, v159 op_sel_hi:[0,0,0]
	s_setprio 0
	s_setprio 1
	s_nop 0
	v_mfma_scale_f32_16x16x128_f8f6f4 v[118:121], v[162:169], v[192:199], v[118:121], v160, v159 op_sel_hi:[0,0,0]
	v_mfma_scale_f32_16x16x128_f8f6f4 v[114:117], v[170:177], v[192:199], v[114:117], v160, v159 op_sel_hi:[0,0,0]
	v_mfma_scale_f32_16x16x128_f8f6f4 v[102:105], v[162:169], v[200:207], v[102:105], v160, v159 op_sel_hi:[0,0,0]
	v_mfma_scale_f32_16x16x128_f8f6f4 v[98:101], v[170:177], v[200:207], v[98:101], v160, v159 op_sel_hi:[0,0,0]
	v_mfma_scale_f32_16x16x128_f8f6f4 v[86:89], v[162:169], v[208:215], v[86:89], v160, v159 op_sel_hi:[0,0,0]
	v_mfma_scale_f32_16x16x128_f8f6f4 v[82:85], v[170:177], v[208:215], v[82:85], v160, v159 op_sel_hi:[0,0,0]
	v_mfma_scale_f32_16x16x128_f8f6f4 v[70:73], v[162:169], v[216:223], v[70:73], v160, v159 op_sel_hi:[0,0,0]
	v_mfma_scale_f32_16x16x128_f8f6f4 v[66:69], v[170:177], v[216:223], v[66:69], v160, v159 op_sel_hi:[0,0,0]
	s_setprio 0
	s_barrier
	s_add_i32 s24, s56, s29
	s_mov_b32 m0, s24
	ds_read_b128 v[192:195], v157 offset:49152
	ds_read_b128 v[196:199], v157 offset:50176
	ds_read_b128 v[200:203], v157 offset:51200
	ds_read_b128 v[204:207], v157 offset:52224
	ds_read_b128 v[208:211], v157 offset:53248
	ds_read_b128 v[212:215], v157 offset:54272
	ds_read_b128 v[216:219], v157 offset:55296
	ds_read_b128 v[220:223], v157 offset:56320
	s_waitcnt vmcnt(2)
	s_waitcnt lgkmcnt(0)
	s_barrier
	s_setprio 1
	s_waitcnt lgkmcnt(0)
	s_nop 0
	v_mfma_scale_f32_16x16x128_f8f6f4 v[62:65], v[2:9], v[192:199], v[62:65], v160, v159 op_sel_hi:[0,0,0]
	global_load_lds_dwordx4 v132, s[90:91]
	s_add_i32 m0, s24, 0x2000
	v_mfma_scale_f32_16x16x128_f8f6f4 v[58:61], v[18:25], v[192:199], v[58:61], v160, v159 op_sel_hi:[0,0,0]
	s_add_u32 s22, s22, 0xb0080
	s_addc_u32 s23, s23, 0
	v_mfma_scale_f32_16x16x128_f8f6f4 v[46:49], v[2:9], v[200:207], v[46:49], v160, v159 op_sel_hi:[0,0,0]
	s_add_i32 s24, s57, s29
	global_load_lds_dwordx4 v136, s[90:91]
	v_mfma_scale_f32_16x16x128_f8f6f4 v[42:45], v[18:25], v[200:207], v[42:45], v160, v159 op_sel_hi:[0,0,0]
	s_mov_b32 m0, s24
	s_nop 0
	v_mfma_scale_f32_16x16x128_f8f6f4 v[30:33], v[2:9], v[208:215], v[30:33], v160, v159 op_sel_hi:[0,0,0]
	global_load_lds_dwordx4 v132, s[22:23]
	s_add_i32 m0, s24, 0x2000
	v_mfma_scale_f32_16x16x128_f8f6f4 v[26:29], v[18:25], v[208:215], v[26:29], v160, v159 op_sel_hi:[0,0,0]
	s_nop 0
	global_load_lds_dwordx4 v136, s[22:23]
	v_mfma_scale_f32_16x16x128_f8f6f4 v[14:17], v[2:9], v[216:223], v[14:17], v160, v159 op_sel_hi:[0,0,0]
	s_mov_b32 m0, s36
	s_nop 0
	v_mfma_scale_f32_16x16x128_f8f6f4 v[10:13], v[18:25], v[216:223], v[10:13], v160, v159 op_sel_hi:[0,0,0]
	global_load_lds_dwordx4 v130, s[92:93]
	s_mov_b32 m0, s37
	s_setprio 0
	s_setprio 1
	s_nop 0
	v_mfma_scale_f32_16x16x128_f8f6f4 v[54:57], v[162:169], v[192:199], v[54:57], v160, v159 op_sel_hi:[0,0,0]
	s_nop 0
	global_load_lds_dwordx4 v134, s[92:93]
	v_mfma_scale_f32_16x16x128_f8f6f4 v[50:53], v[170:177], v[192:199], v[50:53], v160, v159 op_sel_hi:[0,0,0]
	v_mfma_scale_f32_16x16x128_f8f6f4 v[38:41], v[162:169], v[200:207], v[38:41], v160, v159 op_sel_hi:[0,0,0]
	v_mfma_scale_f32_16x16x128_f8f6f4 v[34:37], v[170:177], v[200:207], v[34:37], v160, v159 op_sel_hi:[0,0,0]
	v_mfma_scale_f32_16x16x128_f8f6f4 v[22:25], v[162:169], v[208:215], v[148:151], v160, v159 op_sel_hi:[0,0,0]
	v_mfma_scale_f32_16x16x128_f8f6f4 v[18:21], v[170:177], v[208:215], v[186:189], v160, v159 op_sel_hi:[0,0,0]
	v_mfma_scale_f32_16x16x128_f8f6f4 v[6:9], v[162:169], v[216:223], v[178:181], v160, v159 op_sel_hi:[0,0,0]
	v_mfma_scale_f32_16x16x128_f8f6f4 v[2:5], v[170:177], v[216:223], v[182:185], v160, v159 op_sel_hi:[0,0,0]
	s_setprio 0
	s_barrier
	s_add_i32 s55, s55, 2
	s_add_u32 s20, s20, 0x100
	s_addc_u32 s21, s21, 0
	s_add_u32 s49, s49, 0x100
	s_addc_u32 s54, s54, 0
	s_cmp_gt_u32 s55, 41
	s_cbranch_scc0 .LBB0_556
	s_and_b64 vcc, exec, s[16:17]
	s_cbranch_vccz .LBB0_559
	s_barrier

.LBB0_651:
	ds_read_b128 v[148:151], v157
	ds_read_b128 v[162:165], v157 offset:1024
	ds_read_b128 v[166:169], v157 offset:2048
	ds_read_b128 v[170:173], v157 offset:3072
	ds_read_b128 v[174:177], v159
	ds_read_b128 v[178:181], v159 offset:1024
	ds_read_b128 v[182:185], v159 offset:2048
	ds_read_b128 v[186:189], v159 offset:3072
	s_add_u32 s36, s34, 0xfff80080
	s_addc_u32 s37, s35, -1
	s_cmp_eq_u32 s66, 28
	s_cselect_b32 s39, s27, s37
	s_cselect_b32 s38, s62, s36
	s_cselect_b32 s37, s25, s65
	s_cselect_b32 s36, s63, s64
	s_add_i32 m0, s42, 0xc000
	ds_read_b128 v[190:193], v160
	ds_read_b128 v[194:197], v160 offset:1024
	ds_read_b128 v[198:201], v160 offset:2048
	ds_read_b128 v[202:205], v160 offset:3072
	ds_read_b128 v[206:209], v160 offset:4096
	ds_read_b128 v[210:213], v160 offset:5120
	ds_read_b128 v[214:217], v160 offset:6144
	ds_read_b128 v[218:221], v160 offset:7168
	s_waitcnt vmcnt(6)
	s_waitcnt lgkmcnt(0)
	s_barrier
	s_setprio 1
	s_waitcnt lgkmcnt(0)
	v_mfma_f32_16x16x32_bf16 v[126:129], v[148:151], v[190:193], v[126:129]
	global_load_lds_dwordx4 v138, s[34:35]
	v_mfma_f32_16x16x32_bf16 v[122:125], v[166:169], v[190:193], v[122:125]
	s_add_i32 m0, s42, 0xe000
	v_mfma_f32_16x16x32_bf16 v[110:113], v[148:151], v[198:201], v[110:113]
	s_nop 0
	v_mfma_f32_16x16x32_bf16 v[106:109], v[166:169], v[198:201], v[106:109]
	global_load_lds_dwordx4 v140, s[34:35]
	v_mfma_f32_16x16x32_bf16 v[94:97], v[148:151], v[206:209], v[94:97]
	v_mfma_f32_16x16x32_bf16 v[90:93], v[166:169], v[206:209], v[90:93]
	v_mfma_f32_16x16x32_bf16 v[78:81], v[148:151], v[214:217], v[78:81]
	v_mfma_f32_16x16x32_bf16 v[74:77], v[166:169], v[214:217], v[74:77]
	v_mfma_f32_16x16x32_bf16 v[126:129], v[162:165], v[194:197], v[126:129]
	v_mfma_f32_16x16x32_bf16 v[122:125], v[170:173], v[194:197], v[122:125]
	v_mfma_f32_16x16x32_bf16 v[110:113], v[162:165], v[202:205], v[110:113]
	v_mfma_f32_16x16x32_bf16 v[106:109], v[170:173], v[202:205], v[106:109]
	v_mfma_f32_16x16x32_bf16 v[94:97], v[162:165], v[210:213], v[94:97]
	v_mfma_f32_16x16x32_bf16 v[90:93], v[170:173], v[210:213], v[90:93]
	v_mfma_f32_16x16x32_bf16 v[78:81], v[162:165], v[218:221], v[78:81]
	v_mfma_f32_16x16x32_bf16 v[74:77], v[170:173], v[218:221], v[74:77]
	s_setprio 0
	s_setprio 1
	v_mfma_f32_16x16x32_bf16 v[118:121], v[174:177], v[190:193], v[118:121]
	v_mfma_f32_16x16x32_bf16 v[114:117], v[182:185], v[190:193], v[114:117]
	v_mfma_f32_16x16x32_bf16 v[102:105], v[174:177], v[198:201], v[102:105]
	v_mfma_f32_16x16x32_bf16 v[98:101], v[182:185], v[198:201], v[98:101]
	v_mfma_f32_16x16x32_bf16 v[86:89], v[174:177], v[206:209], v[86:89]
	v_mfma_f32_16x16x32_bf16 v[82:85], v[182:185], v[206:209], v[82:85]
	v_mfma_f32_16x16x32_bf16 v[70:73], v[174:177], v[214:217], v[70:73]
	v_mfma_f32_16x16x32_bf16 v[66:69], v[182:185], v[214:217], v[66:69]
	v_mfma_f32_16x16x32_bf16 v[118:121], v[178:181], v[194:197], v[118:121]
	v_mfma_f32_16x16x32_bf16 v[114:117], v[186:189], v[194:197], v[114:117]
	v_mfma_f32_16x16x32_bf16 v[102:105], v[178:181], v[202:205], v[102:105]
	v_mfma_f32_16x16x32_bf16 v[98:101], v[186:189], v[202:205], v[98:101]
	v_mfma_f32_16x16x32_bf16 v[86:89], v[178:181], v[210:213], v[86:89]
	v_mfma_f32_16x16x32_bf16 v[82:85], v[186:189], v[210:213], v[82:85]
	v_mfma_f32_16x16x32_bf16 v[70:73], v[178:181], v[218:221], v[70:73]
	v_mfma_f32_16x16x32_bf16 v[66:69], v[186:189], v[218:221], v[66:69]
	s_setprio 0
	s_barrier
	s_add_i32 s67, s56, s41
	s_add_u32 s90, s36, s14
	s_addc_u32 s91, s37, s15
	s_mov_b32 m0, s67
	ds_read_b128 v[190:193], v160 offset:16384
	ds_read_b128 v[194:197], v160 offset:17408
	ds_read_b128 v[198:201], v160 offset:18432
	ds_read_b128 v[202:205], v160 offset:19456
	ds_read_b128 v[206:209], v160 offset:20480
	ds_read_b128 v[210:213], v160 offset:21504
	ds_read_b128 v[214:217], v160 offset:22528
	ds_read_b128 v[218:221], v160 offset:23552
	s_waitcnt vmcnt(2)
	s_waitcnt lgkmcnt(0)
	s_barrier
	s_setprio 1
	s_waitcnt lgkmcnt(0)
	v_mfma_f32_16x16x32_bf16 v[62:65], v[148:151], v[190:193], v[62:65]
	global_load_lds_dwordx4 v132, s[36:37]
	v_mfma_f32_16x16x32_bf16 v[58:61], v[166:169], v[190:193], v[58:61]
	s_add_i32 m0, s67, 0x2000
	v_mfma_f32_16x16x32_bf16 v[46:49], v[148:151], v[198:201], v[46:49]
	s_add_u32 s68, s36, 0x80000
	v_mfma_f32_16x16x32_bf16 v[42:45], v[166:169], v[198:201], v[42:45]
	s_addc_u32 s69, s37, 0
	v_mfma_f32_16x16x32_bf16 v[30:33], v[148:151], v[206:209], v[30:33]
	s_add_i32 s67, s57, s41
	v_mfma_f32_16x16x32_bf16 v[26:29], v[166:169], v[206:209], v[26:29]
	global_load_lds_dwordx4 v136, s[36:37]
	v_mfma_f32_16x16x32_bf16 v[14:17], v[148:151], v[214:217], v[14:17]
	s_mov_b32 m0, s67
	v_mfma_f32_16x16x32_bf16 v[10:13], v[166:169], v[214:217], v[10:13]
	s_nop 0
	v_mfma_f32_16x16x32_bf16 v[62:65], v[162:165], v[194:197], v[62:65]
	global_load_lds_dwordx4 v132, s[68:69]
	v_mfma_f32_16x16x32_bf16 v[58:61], v[170:173], v[194:197], v[58:61]
	s_add_i32 m0, s67, 0x2000
	v_mfma_f32_16x16x32_bf16 v[46:49], v[162:165], v[202:205], v[46:49]
	s_nop 0
	v_mfma_f32_16x16x32_bf16 v[42:45], v[170:173], v[202:205], v[42:45]
	global_load_lds_dwordx4 v136, s[68:69]
	v_mfma_f32_16x16x32_bf16 v[30:33], v[162:165], v[210:213], v[30:33]
	s_add_u32 s92, s38, s14
	v_mfma_f32_16x16x32_bf16 v[26:29], v[170:173], v[210:213], v[26:29]
	s_addc_u32 s93, s39, s15
	v_mfma_f32_16x16x32_bf16 v[14:17], v[162:165], v[218:221], v[14:17]
	s_mov_b32 m0, s42
	v_mfma_f32_16x16x32_bf16 v[10:13], v[170:173], v[218:221], v[10:13]
	s_nop 0
	s_setprio 0
	s_setprio 1
	v_mfma_f32_16x16x32_bf16 v[54:57], v[174:177], v[190:193], v[54:57]
	global_load_lds_dwordx4 v130, s[38:39]
	v_mfma_f32_16x16x32_bf16 v[50:53], v[182:185], v[190:193], v[50:53]
	s_mov_b32 m0, s43
	v_mfma_f32_16x16x32_bf16 v[38:41], v[174:177], v[198:201], v[38:41]
	s_nop 0
	v_mfma_f32_16x16x32_bf16 v[34:37], v[182:185], v[198:201], v[34:37]
	global_load_lds_dwordx4 v134, s[38:39]
	v_mfma_f32_16x16x32_bf16 v[22:25], v[174:177], v[206:209], v[22:25]
	v_mfma_f32_16x16x32_bf16 v[18:21], v[182:185], v[206:209], v[18:21]
	v_mfma_f32_16x16x32_bf16 v[6:9], v[174:177], v[214:217], v[6:9]
	v_mfma_f32_16x16x32_bf16 v[2:5], v[182:185], v[214:217], v[2:5]
	v_mfma_f32_16x16x32_bf16 v[54:57], v[178:181], v[194:197], v[54:57]
	v_mfma_f32_16x16x32_bf16 v[50:53], v[186:189], v[194:197], v[50:53]
	v_mfma_f32_16x16x32_bf16 v[38:41], v[178:181], v[202:205], v[38:41]
	v_mfma_f32_16x16x32_bf16 v[34:37], v[186:189], v[202:205], v[34:37]
	v_mfma_f32_16x16x32_bf16 v[22:25], v[178:181], v[210:213], v[22:25]
	v_mfma_f32_16x16x32_bf16 v[18:21], v[186:189], v[210:213], v[18:21]
	v_mfma_f32_16x16x32_bf16 v[6:9], v[178:181], v[218:221], v[6:9]
	v_mfma_f32_16x16x32_bf16 v[2:5], v[186:189], v[218:221], v[2:5]
	s_setprio 0
	s_barrier
	s_add_i32 s67, 0, 0x18000
	s_add_i32 s68, 0, 0x1c000
	v_add_u32_e32 v170, s67, v155
	v_add_u32_e32 v186, s68, v155
	ds_read_b128 v[148:151], v170
	ds_read_b128 v[162:165], v170 offset:1024
	ds_read_b128 v[166:169], v170 offset:2048
	ds_read_b128 v[170:173], v170 offset:3072
	ds_read_b128 v[174:177], v186
	ds_read_b128 v[178:181], v186 offset:1024
	ds_read_b128 v[182:185], v186 offset:2048
	ds_read_b128 v[186:189], v186 offset:3072
	s_add_u32 s38, s38, 0x80000
	s_addc_u32 s39, s39, 0
	s_mov_b32 m0, s44
	ds_read_b128 v[190:193], v160 offset:32768
	ds_read_b128 v[194:197], v160 offset:33792
	ds_read_b128 v[198:201], v160 offset:34816
	ds_read_b128 v[202:205], v160 offset:35840
	ds_read_b128 v[206:209], v160 offset:36864
	ds_read_b128 v[210:213], v160 offset:37888
	ds_read_b128 v[214:217], v160 offset:38912
	ds_read_b128 v[218:221], v160 offset:39936
	s_waitcnt vmcnt(6)
	s_waitcnt lgkmcnt(0)
	s_barrier
	s_setprio 1
	s_waitcnt lgkmcnt(0)
	v_mfma_f32_16x16x32_bf16 v[126:129], v[148:151], v[190:193], v[126:129]
	global_load_lds_dwordx4 v130, s[38:39]
	v_mfma_f32_16x16x32_bf16 v[122:125], v[166:169], v[190:193], v[122:125]
	s_mov_b32 m0, s45
	v_mfma_f32_16x16x32_bf16 v[110:113], v[148:151], v[198:201], v[110:113]
	s_nop 0
	v_mfma_f32_16x16x32_bf16 v[106:109], v[166:169], v[198:201], v[106:109]
	global_load_lds_dwordx4 v134, s[38:39]
	v_mfma_f32_16x16x32_bf16 v[94:97], v[148:151], v[206:209], v[94:97]
	v_mfma_f32_16x16x32_bf16 v[90:93], v[166:169], v[206:209], v[90:93]
	v_mfma_f32_16x16x32_bf16 v[78:81], v[148:151], v[214:217], v[78:81]
	v_mfma_f32_16x16x32_bf16 v[74:77], v[166:169], v[214:217], v[74:77]
	v_mfma_f32_16x16x32_bf16 v[126:129], v[162:165], v[194:197], v[126:129]
	v_mfma_f32_16x16x32_bf16 v[122:125], v[170:173], v[194:197], v[122:125]
	v_mfma_f32_16x16x32_bf16 v[110:113], v[162:165], v[202:205], v[110:113]
	v_mfma_f32_16x16x32_bf16 v[106:109], v[170:173], v[202:205], v[106:109]
	v_mfma_f32_16x16x32_bf16 v[94:97], v[162:165], v[210:213], v[94:97]
	v_mfma_f32_16x16x32_bf16 v[90:93], v[170:173], v[210:213], v[90:93]
	v_mfma_f32_16x16x32_bf16 v[78:81], v[162:165], v[218:221], v[78:81]
	v_mfma_f32_16x16x32_bf16 v[74:77], v[170:173], v[218:221], v[74:77]
	s_setprio 0
	s_setprio 1
	v_mfma_f32_16x16x32_bf16 v[118:121], v[174:177], v[190:193], v[118:121]
	v_mfma_f32_16x16x32_bf16 v[114:117], v[182:185], v[190:193], v[114:117]
	v_mfma_f32_16x16x32_bf16 v[102:105], v[174:177], v[198:201], v[102:105]
	v_mfma_f32_16x16x32_bf16 v[98:101], v[182:185], v[198:201], v[98:101]
	v_mfma_f32_16x16x32_bf16 v[86:89], v[174:177], v[206:209], v[86:89]
	v_mfma_f32_16x16x32_bf16 v[82:85], v[182:185], v[206:209], v[82:85]
	v_mfma_f32_16x16x32_bf16 v[70:73], v[174:177], v[214:217], v[70:73]
	v_mfma_f32_16x16x32_bf16 v[66:69], v[182:185], v[214:217], v[66:69]
	v_mfma_f32_16x16x32_bf16 v[118:121], v[178:181], v[194:197], v[118:121]
	v_mfma_f32_16x16x32_bf16 v[114:117], v[186:189], v[194:197], v[114:117]
	v_mfma_f32_16x16x32_bf16 v[102:105], v[178:181], v[202:205], v[102:105]
	v_mfma_f32_16x16x32_bf16 v[98:101], v[186:189], v[202:205], v[98:101]
	v_mfma_f32_16x16x32_bf16 v[86:89], v[178:181], v[210:213], v[86:89]
	v_mfma_f32_16x16x32_bf16 v[82:85], v[186:189], v[210:213], v[82:85]
	v_mfma_f32_16x16x32_bf16 v[70:73], v[178:181], v[218:221], v[70:73]
	v_mfma_f32_16x16x32_bf16 v[66:69], v[186:189], v[218:221], v[66:69]
	s_setprio 0
	s_barrier
	s_add_i32 s38, s67, s41
	s_mov_b32 m0, s38
	ds_read_b128 v[190:193], v160 offset:49152
	ds_read_b128 v[194:197], v160 offset:50176
	ds_read_b128 v[198:201], v160 offset:51200
	ds_read_b128 v[202:205], v160 offset:52224
	ds_read_b128 v[206:209], v160 offset:53248
	ds_read_b128 v[210:213], v160 offset:54272
	ds_read_b128 v[214:217], v160 offset:55296
	ds_read_b128 v[218:221], v160 offset:56320
	s_waitcnt vmcnt(2)
	s_waitcnt lgkmcnt(0)
	s_barrier
	s_setprio 1
	s_waitcnt lgkmcnt(0)
	v_mfma_f32_16x16x32_bf16 v[62:65], v[148:151], v[190:193], v[62:65]
	global_load_lds_dwordx4 v132, s[90:91]
	v_mfma_f32_16x16x32_bf16 v[58:61], v[166:169], v[190:193], v[58:61]
	s_add_i32 m0, s38, 0x2000
	v_mfma_f32_16x16x32_bf16 v[46:49], v[148:151], v[198:201], v[46:49]
	s_add_u32 s36, s36, 0x80080
	v_mfma_f32_16x16x32_bf16 v[42:45], v[166:169], v[198:201], v[42:45]
	s_addc_u32 s37, s37, 0
	v_mfma_f32_16x16x32_bf16 v[30:33], v[148:151], v[206:209], v[30:33]
	s_add_i32 s38, s68, s41
	v_mfma_f32_16x16x32_bf16 v[26:29], v[166:169], v[206:209], v[26:29]
	global_load_lds_dwordx4 v136, s[90:91]
	v_mfma_f32_16x16x32_bf16 v[14:17], v[148:151], v[214:217], v[14:17]
	s_mov_b32 m0, s38
	v_mfma_f32_16x16x32_bf16 v[10:13], v[166:169], v[214:217], v[10:13]
	s_nop 0
	v_mfma_f32_16x16x32_bf16 v[62:65], v[162:165], v[194:197], v[62:65]
	global_load_lds_dwordx4 v132, s[36:37]
	v_mfma_f32_16x16x32_bf16 v[58:61], v[170:173], v[194:197], v[58:61]
	s_add_i32 m0, s38, 0x2000
	v_mfma_f32_16x16x32_bf16 v[46:49], v[162:165], v[202:205], v[46:49]
	s_nop 0
	v_mfma_f32_16x16x32_bf16 v[42:45], v[170:173], v[202:205], v[42:45]
	global_load_lds_dwordx4 v136, s[36:37]
	v_mfma_f32_16x16x32_bf16 v[30:33], v[162:165], v[210:213], v[30:33]
	s_mov_b32 m0, s49
	v_mfma_f32_16x16x32_bf16 v[26:29], v[170:173], v[210:213], v[26:29]
	s_nop 0
	v_mfma_f32_16x16x32_bf16 v[14:17], v[162:165], v[218:221], v[14:17]
	global_load_lds_dwordx4 v130, s[92:93]
	v_mfma_f32_16x16x32_bf16 v[10:13], v[170:173], v[218:221], v[10:13]
	s_mov_b32 m0, s54
	s_setprio 0
	s_setprio 1
	v_mfma_f32_16x16x32_bf16 v[54:57], v[174:177], v[190:193], v[54:57]
	s_nop 0
	v_mfma_f32_16x16x32_bf16 v[50:53], v[182:185], v[190:193], v[50:53]
	global_load_lds_dwordx4 v134, s[92:93]
	v_mfma_f32_16x16x32_bf16 v[38:41], v[174:177], v[198:201], v[38:41]
	v_mfma_f32_16x16x32_bf16 v[34:37], v[182:185], v[198:201], v[34:37]
	v_mfma_f32_16x16x32_bf16 v[22:25], v[174:177], v[206:209], v[22:25]
	v_mfma_f32_16x16x32_bf16 v[18:21], v[182:185], v[206:209], v[18:21]
	v_mfma_f32_16x16x32_bf16 v[6:9], v[174:177], v[214:217], v[6:9]
	v_mfma_f32_16x16x32_bf16 v[2:5], v[182:185], v[214:217], v[2:5]
	v_mfma_f32_16x16x32_bf16 v[54:57], v[178:181], v[194:197], v[54:57]
	v_mfma_f32_16x16x32_bf16 v[50:53], v[186:189], v[194:197], v[50:53]
	v_mfma_f32_16x16x32_bf16 v[38:41], v[178:181], v[202:205], v[38:41]
	v_mfma_f32_16x16x32_bf16 v[34:37], v[186:189], v[202:205], v[34:37]
	v_mfma_f32_16x16x32_bf16 v[22:25], v[178:181], v[210:213], v[22:25]
	v_mfma_f32_16x16x32_bf16 v[18:21], v[186:189], v[210:213], v[18:21]
	v_mfma_f32_16x16x32_bf16 v[6:9], v[178:181], v[218:221], v[6:9]
	v_mfma_f32_16x16x32_bf16 v[2:5], v[186:189], v[218:221], v[2:5]
	s_setprio 0
	s_barrier
	s_add_i32 s66, s66, 2
	s_add_u32 s34, s34, 0x100
	s_addc_u32 s35, s35, 0
	s_add_u32 s64, s64, 0x100
	s_addc_u32 s65, s65, 0
	s_cmp_gt_u32 s66, 29
	s_cbranch_scc0 .LBB0_651
	s_and_b64 vcc, exec, s[16:17]
	s_cbranch_vccz .LBB0_654
	s_barrier

.LBB0_848:
	ds_read_b128 v[148:151], v157
	ds_read_b128 v[162:165], v157 offset:1024
	ds_read_b128 v[166:169], v157 offset:2048
	ds_read_b128 v[170:173], v157 offset:3072
	ds_read_b128 v[174:177], v159
	ds_read_b128 v[178:181], v159 offset:1024
	ds_read_b128 v[182:185], v159 offset:2048
	ds_read_b128 v[186:189], v159 offset:3072
	s_add_u32 s36, s34, 0xfff80080
	s_addc_u32 s37, s35, -1
	s_cmp_eq_u32 s62, 28
	s_cselect_b32 s39, s23, s37
	s_cselect_b32 s38, s58, s36
	s_cselect_b32 s37, s21, s61
	s_cselect_b32 s36, s59, s60
	s_add_i32 m0, s31, 0xc000
	ds_read_b128 v[190:193], v160
	ds_read_b128 v[194:197], v160 offset:1024
	ds_read_b128 v[198:201], v160 offset:2048
	ds_read_b128 v[202:205], v160 offset:3072
	ds_read_b128 v[206:209], v160 offset:4096
	ds_read_b128 v[210:213], v160 offset:5120
	ds_read_b128 v[214:217], v160 offset:6144
	ds_read_b128 v[218:221], v160 offset:7168
	s_waitcnt vmcnt(6)
	s_waitcnt lgkmcnt(0)
	s_barrier
	s_setprio 1
	s_waitcnt lgkmcnt(0)
	v_mfma_f32_16x16x32_bf16 v[126:129], v[148:151], v[190:193], v[126:129]
	global_load_lds_dwordx4 v138, s[34:35]
	v_mfma_f32_16x16x32_bf16 v[122:125], v[166:169], v[190:193], v[122:125]
	s_add_i32 m0, s31, 0xe000
	v_mfma_f32_16x16x32_bf16 v[110:113], v[148:151], v[198:201], v[110:113]
	s_nop 0
	v_mfma_f32_16x16x32_bf16 v[106:109], v[166:169], v[198:201], v[106:109]
	global_load_lds_dwordx4 v140, s[34:35]
	v_mfma_f32_16x16x32_bf16 v[94:97], v[148:151], v[206:209], v[94:97]
	v_mfma_f32_16x16x32_bf16 v[90:93], v[166:169], v[206:209], v[90:93]
	v_mfma_f32_16x16x32_bf16 v[78:81], v[148:151], v[214:217], v[78:81]
	v_mfma_f32_16x16x32_bf16 v[74:77], v[166:169], v[214:217], v[74:77]
	v_mfma_f32_16x16x32_bf16 v[126:129], v[162:165], v[194:197], v[126:129]
	v_mfma_f32_16x16x32_bf16 v[122:125], v[170:173], v[194:197], v[122:125]
	v_mfma_f32_16x16x32_bf16 v[110:113], v[162:165], v[202:205], v[110:113]
	v_mfma_f32_16x16x32_bf16 v[106:109], v[170:173], v[202:205], v[106:109]
	v_mfma_f32_16x16x32_bf16 v[94:97], v[162:165], v[210:213], v[94:97]
	v_mfma_f32_16x16x32_bf16 v[90:93], v[170:173], v[210:213], v[90:93]
	v_mfma_f32_16x16x32_bf16 v[78:81], v[162:165], v[218:221], v[78:81]
	v_mfma_f32_16x16x32_bf16 v[74:77], v[170:173], v[218:221], v[74:77]
	s_setprio 0
	s_setprio 1
	v_mfma_f32_16x16x32_bf16 v[118:121], v[174:177], v[190:193], v[118:121]
	v_mfma_f32_16x16x32_bf16 v[114:117], v[182:185], v[190:193], v[114:117]
	v_mfma_f32_16x16x32_bf16 v[102:105], v[174:177], v[198:201], v[102:105]
	v_mfma_f32_16x16x32_bf16 v[98:101], v[182:185], v[198:201], v[98:101]
	v_mfma_f32_16x16x32_bf16 v[86:89], v[174:177], v[206:209], v[86:89]
	v_mfma_f32_16x16x32_bf16 v[82:85], v[182:185], v[206:209], v[82:85]
	v_mfma_f32_16x16x32_bf16 v[70:73], v[174:177], v[214:217], v[70:73]
	v_mfma_f32_16x16x32_bf16 v[66:69], v[182:185], v[214:217], v[66:69]
	v_mfma_f32_16x16x32_bf16 v[118:121], v[178:181], v[194:197], v[118:121]
	v_mfma_f32_16x16x32_bf16 v[114:117], v[186:189], v[194:197], v[114:117]
	v_mfma_f32_16x16x32_bf16 v[102:105], v[178:181], v[202:205], v[102:105]
	v_mfma_f32_16x16x32_bf16 v[98:101], v[186:189], v[202:205], v[98:101]
	v_mfma_f32_16x16x32_bf16 v[86:89], v[178:181], v[210:213], v[86:89]
	v_mfma_f32_16x16x32_bf16 v[82:85], v[186:189], v[210:213], v[82:85]
	v_mfma_f32_16x16x32_bf16 v[70:73], v[178:181], v[218:221], v[70:73]
	v_mfma_f32_16x16x32_bf16 v[66:69], v[186:189], v[218:221], v[66:69]
	s_setprio 0
	s_barrier
	s_add_i32 s63, s55, s41
	s_add_u32 s90, s36, s8
	s_addc_u32 s91, s37, s9
	s_mov_b32 m0, s63
	ds_read_b128 v[190:193], v160 offset:16384
	ds_read_b128 v[194:197], v160 offset:17408
	ds_read_b128 v[198:201], v160 offset:18432
	ds_read_b128 v[202:205], v160 offset:19456
	ds_read_b128 v[206:209], v160 offset:20480
	ds_read_b128 v[210:213], v160 offset:21504
	ds_read_b128 v[214:217], v160 offset:22528
	ds_read_b128 v[218:221], v160 offset:23552
	s_waitcnt vmcnt(2)
	s_waitcnt lgkmcnt(0)
	s_barrier
	s_setprio 1
	s_waitcnt lgkmcnt(0)
	v_mfma_f32_16x16x32_bf16 v[62:65], v[148:151], v[190:193], v[62:65]
	global_load_lds_dwordx4 v132, s[36:37]
	v_mfma_f32_16x16x32_bf16 v[58:61], v[166:169], v[190:193], v[58:61]
	s_add_i32 m0, s63, 0x2000
	v_mfma_f32_16x16x32_bf16 v[46:49], v[148:151], v[198:201], v[46:49]
	s_add_u32 s64, s36, 0x80000
	v_mfma_f32_16x16x32_bf16 v[42:45], v[166:169], v[198:201], v[42:45]
	s_addc_u32 s65, s37, 0
	v_mfma_f32_16x16x32_bf16 v[30:33], v[148:151], v[206:209], v[30:33]
	s_add_i32 s63, s56, s41
	v_mfma_f32_16x16x32_bf16 v[26:29], v[166:169], v[206:209], v[26:29]
	global_load_lds_dwordx4 v136, s[36:37]
	v_mfma_f32_16x16x32_bf16 v[14:17], v[148:151], v[214:217], v[14:17]
	s_mov_b32 m0, s63
	v_mfma_f32_16x16x32_bf16 v[10:13], v[166:169], v[214:217], v[10:13]
	s_nop 0
	v_mfma_f32_16x16x32_bf16 v[62:65], v[162:165], v[194:197], v[62:65]
	global_load_lds_dwordx4 v132, s[64:65]
	v_mfma_f32_16x16x32_bf16 v[58:61], v[170:173], v[194:197], v[58:61]
	s_add_i32 m0, s63, 0x2000
	v_mfma_f32_16x16x32_bf16 v[46:49], v[162:165], v[202:205], v[46:49]
	s_nop 0
	v_mfma_f32_16x16x32_bf16 v[42:45], v[170:173], v[202:205], v[42:45]
	global_load_lds_dwordx4 v136, s[64:65]
	v_mfma_f32_16x16x32_bf16 v[30:33], v[162:165], v[210:213], v[30:33]
	s_add_u32 s92, s38, s8
	v_mfma_f32_16x16x32_bf16 v[26:29], v[170:173], v[210:213], v[26:29]
	s_addc_u32 s93, s39, s9
	v_mfma_f32_16x16x32_bf16 v[14:17], v[162:165], v[218:221], v[14:17]
	s_mov_b32 m0, s31
	v_mfma_f32_16x16x32_bf16 v[10:13], v[170:173], v[218:221], v[10:13]
	s_nop 0
	s_setprio 0
	s_setprio 1
	v_mfma_f32_16x16x32_bf16 v[54:57], v[174:177], v[190:193], v[54:57]
	global_load_lds_dwordx4 v130, s[38:39]
	v_mfma_f32_16x16x32_bf16 v[50:53], v[182:185], v[190:193], v[50:53]
	s_mov_b32 m0, s42
	v_mfma_f32_16x16x32_bf16 v[38:41], v[174:177], v[198:201], v[38:41]
	s_nop 0
	v_mfma_f32_16x16x32_bf16 v[34:37], v[182:185], v[198:201], v[34:37]
	global_load_lds_dwordx4 v134, s[38:39]
	v_mfma_f32_16x16x32_bf16 v[22:25], v[174:177], v[206:209], v[22:25]
	v_mfma_f32_16x16x32_bf16 v[18:21], v[182:185], v[206:209], v[18:21]
	v_mfma_f32_16x16x32_bf16 v[6:9], v[174:177], v[214:217], v[6:9]
	v_mfma_f32_16x16x32_bf16 v[2:5], v[182:185], v[214:217], v[2:5]
	v_mfma_f32_16x16x32_bf16 v[54:57], v[178:181], v[194:197], v[54:57]
	v_mfma_f32_16x16x32_bf16 v[50:53], v[186:189], v[194:197], v[50:53]
	v_mfma_f32_16x16x32_bf16 v[38:41], v[178:181], v[202:205], v[38:41]
	v_mfma_f32_16x16x32_bf16 v[34:37], v[186:189], v[202:205], v[34:37]
	v_mfma_f32_16x16x32_bf16 v[22:25], v[178:181], v[210:213], v[22:25]
	v_mfma_f32_16x16x32_bf16 v[18:21], v[186:189], v[210:213], v[18:21]
	v_mfma_f32_16x16x32_bf16 v[6:9], v[178:181], v[218:221], v[6:9]
	v_mfma_f32_16x16x32_bf16 v[2:5], v[186:189], v[218:221], v[2:5]
	s_setprio 0
	s_barrier
	s_add_i32 s63, 0, 0x18000
	v_add_u32_e32 v161, s63, v155
	s_add_i32 s64, 0, 0x1c000
	ds_read_b128 v[148:151], v161
	ds_read_b128 v[162:165], v161 offset:1024
	ds_read_b128 v[166:169], v161 offset:2048
	ds_read_b128 v[170:173], v161 offset:3072
	v_add_u32_e32 v161, s64, v155
	ds_read_b128 v[174:177], v161
	ds_read_b128 v[178:181], v161 offset:1024
	ds_read_b128 v[182:185], v161 offset:2048
	ds_read_b128 v[186:189], v161 offset:3072
	s_add_u32 s38, s38, 0x80000
	s_addc_u32 s39, s39, 0
	s_mov_b32 m0, s43
	ds_read_b128 v[190:193], v160 offset:32768
	ds_read_b128 v[194:197], v160 offset:33792
	ds_read_b128 v[198:201], v160 offset:34816
	ds_read_b128 v[202:205], v160 offset:35840
	ds_read_b128 v[206:209], v160 offset:36864
	ds_read_b128 v[210:213], v160 offset:37888
	ds_read_b128 v[214:217], v160 offset:38912
	ds_read_b128 v[218:221], v160 offset:39936
	s_waitcnt vmcnt(6)
	s_waitcnt lgkmcnt(0)
	s_barrier
	s_setprio 1
	s_waitcnt lgkmcnt(0)
	v_mfma_f32_16x16x32_bf16 v[126:129], v[148:151], v[190:193], v[126:129]
	global_load_lds_dwordx4 v130, s[38:39]
	v_mfma_f32_16x16x32_bf16 v[122:125], v[166:169], v[190:193], v[122:125]
	s_mov_b32 m0, s44
	v_mfma_f32_16x16x32_bf16 v[110:113], v[148:151], v[198:201], v[110:113]
	s_nop 0
	v_mfma_f32_16x16x32_bf16 v[106:109], v[166:169], v[198:201], v[106:109]
	global_load_lds_dwordx4 v134, s[38:39]
	v_mfma_f32_16x16x32_bf16 v[94:97], v[148:151], v[206:209], v[94:97]
	v_mfma_f32_16x16x32_bf16 v[90:93], v[166:169], v[206:209], v[90:93]
	v_mfma_f32_16x16x32_bf16 v[78:81], v[148:151], v[214:217], v[78:81]
	v_mfma_f32_16x16x32_bf16 v[74:77], v[166:169], v[214:217], v[74:77]
	v_mfma_f32_16x16x32_bf16 v[126:129], v[162:165], v[194:197], v[126:129]
	v_mfma_f32_16x16x32_bf16 v[122:125], v[170:173], v[194:197], v[122:125]
	v_mfma_f32_16x16x32_bf16 v[110:113], v[162:165], v[202:205], v[110:113]
	v_mfma_f32_16x16x32_bf16 v[106:109], v[170:173], v[202:205], v[106:109]
	v_mfma_f32_16x16x32_bf16 v[94:97], v[162:165], v[210:213], v[94:97]
	v_mfma_f32_16x16x32_bf16 v[90:93], v[170:173], v[210:213], v[90:93]
	v_mfma_f32_16x16x32_bf16 v[78:81], v[162:165], v[218:221], v[78:81]
	v_mfma_f32_16x16x32_bf16 v[74:77], v[170:173], v[218:221], v[74:77]
	s_setprio 0
	s_setprio 1
	v_mfma_f32_16x16x32_bf16 v[118:121], v[174:177], v[190:193], v[118:121]
	v_mfma_f32_16x16x32_bf16 v[114:117], v[182:185], v[190:193], v[114:117]
	v_mfma_f32_16x16x32_bf16 v[102:105], v[174:177], v[198:201], v[102:105]
	v_mfma_f32_16x16x32_bf16 v[98:101], v[182:185], v[198:201], v[98:101]
	v_mfma_f32_16x16x32_bf16 v[86:89], v[174:177], v[206:209], v[86:89]
	v_mfma_f32_16x16x32_bf16 v[82:85], v[182:185], v[206:209], v[82:85]
	v_mfma_f32_16x16x32_bf16 v[70:73], v[174:177], v[214:217], v[70:73]
	v_mfma_f32_16x16x32_bf16 v[66:69], v[182:185], v[214:217], v[66:69]
	v_mfma_f32_16x16x32_bf16 v[118:121], v[178:181], v[194:197], v[118:121]
	v_mfma_f32_16x16x32_bf16 v[114:117], v[186:189], v[194:197], v[114:117]
	v_mfma_f32_16x16x32_bf16 v[102:105], v[178:181], v[202:205], v[102:105]
	v_mfma_f32_16x16x32_bf16 v[98:101], v[186:189], v[202:205], v[98:101]
	v_mfma_f32_16x16x32_bf16 v[86:89], v[178:181], v[210:213], v[86:89]
	v_mfma_f32_16x16x32_bf16 v[82:85], v[186:189], v[210:213], v[82:85]
	v_mfma_f32_16x16x32_bf16 v[70:73], v[178:181], v[218:221], v[70:73]
	v_mfma_f32_16x16x32_bf16 v[66:69], v[186:189], v[218:221], v[66:69]
	s_setprio 0
	s_barrier
	s_add_i32 s38, s63, s41
	s_mov_b32 m0, s38
	ds_read_b128 v[190:193], v160 offset:49152
	ds_read_b128 v[194:197], v160 offset:50176
	ds_read_b128 v[198:201], v160 offset:51200
	ds_read_b128 v[202:205], v160 offset:52224
	ds_read_b128 v[206:209], v160 offset:53248
	ds_read_b128 v[210:213], v160 offset:54272
	ds_read_b128 v[214:217], v160 offset:55296
	ds_read_b128 v[218:221], v160 offset:56320
	s_waitcnt vmcnt(2)
	s_waitcnt lgkmcnt(0)
	s_barrier
	s_setprio 1
	s_waitcnt lgkmcnt(0)
	v_mfma_f32_16x16x32_bf16 v[62:65], v[148:151], v[190:193], v[62:65]
	global_load_lds_dwordx4 v132, s[90:91]
	v_mfma_f32_16x16x32_bf16 v[58:61], v[166:169], v[190:193], v[58:61]
	s_add_i32 m0, s38, 0x2000
	v_mfma_f32_16x16x32_bf16 v[46:49], v[148:151], v[198:201], v[46:49]
	s_add_u32 s36, s36, 0x80080
	v_mfma_f32_16x16x32_bf16 v[42:45], v[166:169], v[198:201], v[42:45]
	s_addc_u32 s37, s37, 0
	v_mfma_f32_16x16x32_bf16 v[30:33], v[148:151], v[206:209], v[30:33]
	s_add_i32 s38, s64, s41
	v_mfma_f32_16x16x32_bf16 v[26:29], v[166:169], v[206:209], v[26:29]
	global_load_lds_dwordx4 v136, s[90:91]
	v_mfma_f32_16x16x32_bf16 v[14:17], v[148:151], v[214:217], v[14:17]
	s_mov_b32 m0, s38
	v_mfma_f32_16x16x32_bf16 v[10:13], v[166:169], v[214:217], v[10:13]
	s_nop 0
	v_mfma_f32_16x16x32_bf16 v[62:65], v[162:165], v[194:197], v[62:65]
	global_load_lds_dwordx4 v132, s[36:37]
	v_mfma_f32_16x16x32_bf16 v[58:61], v[170:173], v[194:197], v[58:61]
	s_add_i32 m0, s38, 0x2000
	v_mfma_f32_16x16x32_bf16 v[46:49], v[162:165], v[202:205], v[46:49]
	s_nop 0
	v_mfma_f32_16x16x32_bf16 v[42:45], v[170:173], v[202:205], v[42:45]
	global_load_lds_dwordx4 v136, s[36:37]
	v_mfma_f32_16x16x32_bf16 v[30:33], v[162:165], v[210:213], v[30:33]
	s_mov_b32 m0, s48
	v_mfma_f32_16x16x32_bf16 v[26:29], v[170:173], v[210:213], v[26:29]
	s_nop 0
	v_mfma_f32_16x16x32_bf16 v[14:17], v[162:165], v[218:221], v[14:17]
	global_load_lds_dwordx4 v130, s[92:93]
	v_mfma_f32_16x16x32_bf16 v[10:13], v[170:173], v[218:221], v[10:13]
	s_mov_b32 m0, s49
	s_setprio 0
	s_setprio 1
	v_mfma_f32_16x16x32_bf16 v[54:57], v[174:177], v[190:193], v[54:57]
	s_nop 0
	v_mfma_f32_16x16x32_bf16 v[50:53], v[182:185], v[190:193], v[50:53]
	global_load_lds_dwordx4 v134, s[92:93]
	v_mfma_f32_16x16x32_bf16 v[38:41], v[174:177], v[198:201], v[38:41]
	v_mfma_f32_16x16x32_bf16 v[34:37], v[182:185], v[198:201], v[34:37]
	v_mfma_f32_16x16x32_bf16 v[22:25], v[174:177], v[206:209], v[22:25]
	v_mfma_f32_16x16x32_bf16 v[18:21], v[182:185], v[206:209], v[18:21]
	v_mfma_f32_16x16x32_bf16 v[6:9], v[174:177], v[214:217], v[6:9]
	v_mfma_f32_16x16x32_bf16 v[2:5], v[182:185], v[214:217], v[2:5]
	v_mfma_f32_16x16x32_bf16 v[54:57], v[178:181], v[194:197], v[54:57]
	v_mfma_f32_16x16x32_bf16 v[50:53], v[186:189], v[194:197], v[50:53]
	v_mfma_f32_16x16x32_bf16 v[38:41], v[178:181], v[202:205], v[38:41]
	v_mfma_f32_16x16x32_bf16 v[34:37], v[186:189], v[202:205], v[34:37]
	v_mfma_f32_16x16x32_bf16 v[22:25], v[178:181], v[210:213], v[22:25]
	v_mfma_f32_16x16x32_bf16 v[18:21], v[186:189], v[210:213], v[18:21]
	v_mfma_f32_16x16x32_bf16 v[6:9], v[178:181], v[218:221], v[6:9]
	v_mfma_f32_16x16x32_bf16 v[2:5], v[186:189], v[218:221], v[2:5]
	s_setprio 0
	s_barrier
	s_add_i32 s62, s62, 2
	s_add_u32 s34, s34, 0x100
	s_addc_u32 s35, s35, 0
	s_add_u32 s60, s60, 0x100
	s_addc_u32 s61, s61, 0
	s_cmp_gt_u32 s62, 29
	s_cbranch_scc0 .LBB0_848
	s_and_b64 vcc, exec, s[10:11]
	s_cbranch_vccz .LBB0_851
	s_barrier

.LBB0_1084:
	ds_read_b128 v[164:167], v152
	ds_read_b128 v[168:171], v152 offset:1024
	ds_read_b128 v[172:175], v152 offset:2048
	ds_read_b128 v[176:179], v152 offset:3072
	ds_read_b128 v[180:183], v153
	ds_read_b128 v[184:187], v153 offset:1024
	ds_read_b128 v[224:227], v153 offset:2048
	ds_read_b128 v[228:231], v153 offset:3072
	s_add_u32 s30, s26, 0xfffc0080
	s_addc_u32 s31, s27, -1
	s_cmp_eq_u32 s63, 12
	s_cselect_b32 s35, s17, s31
	s_cselect_b32 s34, s59, s30
	s_cselect_b32 s31, s19, s62
	s_cselect_b32 s30, s60, s61
	s_add_i32 m0, s25, 0xc000
	ds_read_b128 v[192:195], v154
	ds_read_b128 v[196:199], v154 offset:1024
	ds_read_b128 v[200:203], v154 offset:2048
	ds_read_b128 v[204:207], v154 offset:3072
	ds_read_b128 v[208:211], v154 offset:4096
	ds_read_b128 v[212:215], v154 offset:5120
	ds_read_b128 v[216:219], v154 offset:6144
	ds_read_b128 v[220:223], v154 offset:7168
	s_waitcnt vmcnt(6)
	s_waitcnt lgkmcnt(0)
	s_barrier
	s_setprio 1
	s_waitcnt lgkmcnt(0)
	s_nop 0
	v_mfma_scale_f32_16x16x128_f8f6f4 v[126:129], v[164:171], v[192:199], v[126:129], v156, v155 op_sel_hi:[0,0,0]
	global_load_lds_dwordx4 v142, s[26:27]
	v_mfma_scale_f32_16x16x128_f8f6f4 v[122:125], v[172:179], v[192:199], v[122:125], v156, v155 op_sel_hi:[0,0,0]
	s_add_i32 m0, s25, 0xe000
	v_mfma_scale_f32_16x16x128_f8f6f4 v[110:113], v[164:171], v[200:207], v[110:113], v156, v155 op_sel_hi:[0,0,0]
	s_nop 0
	v_mfma_scale_f32_16x16x128_f8f6f4 v[106:109], v[172:179], v[200:207], v[106:109], v156, v155 op_sel_hi:[0,0,0]
	global_load_lds_dwordx4 v144, s[26:27]
	v_mfma_scale_f32_16x16x128_f8f6f4 v[94:97], v[164:171], v[208:215], v[94:97], v156, v155 op_sel_hi:[0,0,0]
	v_mfma_scale_f32_16x16x128_f8f6f4 v[90:93], v[172:179], v[208:215], v[90:93], v156, v155 op_sel_hi:[0,0,0]
	v_mfma_scale_f32_16x16x128_f8f6f4 v[78:81], v[164:171], v[216:223], v[78:81], v156, v155 op_sel_hi:[0,0,0]
	v_mfma_scale_f32_16x16x128_f8f6f4 v[74:77], v[172:179], v[216:223], v[74:77], v156, v155 op_sel_hi:[0,0,0]
	s_setprio 0
	s_setprio 1
	s_nop 0
	v_mfma_scale_f32_16x16x128_f8f6f4 v[118:121], v[180:187], v[192:199], v[118:121], v156, v155 op_sel_hi:[0,0,0]
	v_mfma_scale_f32_16x16x128_f8f6f4 v[114:117], v[224:231], v[192:199], v[114:117], v156, v155 op_sel_hi:[0,0,0]
	v_mfma_scale_f32_16x16x128_f8f6f4 v[102:105], v[180:187], v[200:207], v[102:105], v156, v155 op_sel_hi:[0,0,0]
	v_mfma_scale_f32_16x16x128_f8f6f4 v[98:101], v[224:231], v[200:207], v[98:101], v156, v155 op_sel_hi:[0,0,0]
	v_mfma_scale_f32_16x16x128_f8f6f4 v[86:89], v[180:187], v[208:215], v[86:89], v156, v155 op_sel_hi:[0,0,0]
	v_mfma_scale_f32_16x16x128_f8f6f4 v[82:85], v[224:231], v[208:215], v[82:85], v156, v155 op_sel_hi:[0,0,0]
	v_mfma_scale_f32_16x16x128_f8f6f4 v[70:73], v[180:187], v[216:223], v[70:73], v156, v155 op_sel_hi:[0,0,0]
	v_mfma_scale_f32_16x16x128_f8f6f4 v[66:69], v[224:231], v[216:223], v[66:69], v156, v155 op_sel_hi:[0,0,0]
	s_setprio 0
	s_barrier
	s_add_i32 s64, s53, s40
	s_add_u32 s90, s30, s8
	s_addc_u32 s91, s31, s9
	s_mov_b32 m0, s64
	ds_read_b128 v[192:195], v154 offset:16384
	ds_read_b128 v[196:199], v154 offset:17408
	ds_read_b128 v[200:203], v154 offset:18432
	ds_read_b128 v[204:207], v154 offset:19456
	ds_read_b128 v[208:211], v154 offset:20480
	ds_read_b128 v[212:215], v154 offset:21504
	ds_read_b128 v[216:219], v154 offset:22528
	ds_read_b128 v[220:223], v154 offset:23552
	s_waitcnt vmcnt(2)
	s_waitcnt lgkmcnt(0)
	s_barrier
	s_setprio 1
	s_waitcnt lgkmcnt(0)
	s_nop 0
	v_mfma_scale_f32_16x16x128_f8f6f4 v[62:65], v[164:171], v[192:199], v[62:65], v156, v155 op_sel_hi:[0,0,0]
	global_load_lds_dwordx4 v132, s[30:31]
	s_add_i32 m0, s64, 0x2000
	v_mfma_scale_f32_16x16x128_f8f6f4 v[58:61], v[172:179], v[192:199], v[58:61], v156, v155 op_sel_hi:[0,0,0]
	s_add_u32 s64, s30, 0x40000
	s_addc_u32 s65, s31, 0
	v_mfma_scale_f32_16x16x128_f8f6f4 v[46:49], v[164:171], v[200:207], v[46:49], v156, v155 op_sel_hi:[0,0,0]
	s_add_i32 s66, s54, s40
	global_load_lds_dwordx4 v140, s[30:31]
	v_mfma_scale_f32_16x16x128_f8f6f4 v[42:45], v[172:179], v[200:207], v[42:45], v156, v155 op_sel_hi:[0,0,0]
	s_mov_b32 m0, s66
	s_add_u32 s92, s34, s8
	v_mfma_scale_f32_16x16x128_f8f6f4 v[30:33], v[164:171], v[208:215], v[30:33], v156, v155 op_sel_hi:[0,0,0]
	s_addc_u32 s93, s35, s9
	s_nop 0
	v_mfma_scale_f32_16x16x128_f8f6f4 v[26:29], v[172:179], v[208:215], v[26:29], v156, v155 op_sel_hi:[0,0,0]
	global_load_lds_dwordx4 v132, s[64:65]
	s_add_i32 m0, s66, 0x2000
	v_mfma_scale_f32_16x16x128_f8f6f4 v[14:17], v[164:171], v[216:223], v[14:17], v156, v155 op_sel_hi:[0,0,0]
	s_nop 0
	global_load_lds_dwordx4 v140, s[64:65]
	v_mfma_scale_f32_16x16x128_f8f6f4 v[10:13], v[172:179], v[216:223], v[10:13], v156, v155 op_sel_hi:[0,0,0]
	s_mov_b32 m0, s25
	s_nop 0
	s_setprio 0
	s_setprio 1
	s_nop 0
	v_mfma_scale_f32_16x16x128_f8f6f4 v[54:57], v[180:187], v[192:199], v[54:57], v156, v155 op_sel_hi:[0,0,0]
	global_load_lds_dwordx4 v138, s[34:35]
	s_mov_b32 m0, s44
	v_mfma_scale_f32_16x16x128_f8f6f4 v[50:53], v[224:231], v[192:199], v[50:53], v156, v155 op_sel_hi:[0,0,0]
	s_nop 0
	global_load_lds_dwordx4 v136, s[34:35]
	v_mfma_scale_f32_16x16x128_f8f6f4 v[38:41], v[180:187], v[200:207], v[38:41], v156, v155 op_sel_hi:[0,0,0]
	v_mfma_scale_f32_16x16x128_f8f6f4 v[34:37], v[224:231], v[200:207], v[34:37], v156, v155 op_sel_hi:[0,0,0]
	v_mfma_scale_f32_16x16x128_f8f6f4 v[148:151], v[180:187], v[208:215], v[22:25], v156, v155 op_sel_hi:[0,0,0]
	v_mfma_scale_f32_16x16x128_f8f6f4 v[158:161], v[224:231], v[208:215], v[18:21], v156, v155 op_sel_hi:[0,0,0]
	v_mfma_scale_f32_16x16x128_f8f6f4 v[180:183], v[180:187], v[216:223], v[6:9], v156, v155 op_sel_hi:[0,0,0]
	v_mfma_scale_f32_16x16x128_f8f6f4 v[184:187], v[224:231], v[216:223], v[2:5], v156, v155 op_sel_hi:[0,0,0]
	s_setprio 0
	s_barrier
	s_add_i32 s64, 0, 0x18000
	s_add_i32 s65, 0, 0x1c000
	v_add_u32_e32 v22, s64, v135
	v_add_u32_e32 v162, s65, v135
	s_nop 0
	ds_read_b128 v[2:5], v22
	ds_read_b128 v[6:9], v22 offset:1024
	ds_read_b128 v[18:21], v22 offset:2048
	ds_read_b128 v[22:25], v22 offset:3072
	ds_read_b128 v[164:167], v162
	ds_read_b128 v[168:171], v162 offset:1024
	ds_read_b128 v[172:175], v162 offset:2048
	ds_read_b128 v[176:179], v162 offset:3072
	s_add_u32 s34, s34, 0x40000
	s_addc_u32 s35, s35, 0
	s_mov_b32 m0, s45
	ds_read_b128 v[192:195], v154 offset:32768
	ds_read_b128 v[196:199], v154 offset:33792
	ds_read_b128 v[200:203], v154 offset:34816
	ds_read_b128 v[204:207], v154 offset:35840
	ds_read_b128 v[208:211], v154 offset:36864
	ds_read_b128 v[212:215], v154 offset:37888
	ds_read_b128 v[216:219], v154 offset:38912
	ds_read_b128 v[220:223], v154 offset:39936
	s_waitcnt vmcnt(6)
	s_waitcnt lgkmcnt(0)
	s_barrier
	s_setprio 1
	s_waitcnt lgkmcnt(0)
	s_nop 0
	v_mfma_scale_f32_16x16x128_f8f6f4 v[126:129], v[2:9], v[192:199], v[126:129], v156, v155 op_sel_hi:[0,0,0]
	global_load_lds_dwordx4 v138, s[34:35]
	v_mfma_scale_f32_16x16x128_f8f6f4 v[122:125], v[18:25], v[192:199], v[122:125], v156, v155 op_sel_hi:[0,0,0]
	s_mov_b32 m0, s48
	v_mfma_scale_f32_16x16x128_f8f6f4 v[110:113], v[2:9], v[200:207], v[110:113], v156, v155 op_sel_hi:[0,0,0]
	s_nop 0
	v_mfma_scale_f32_16x16x128_f8f6f4 v[106:109], v[18:25], v[200:207], v[106:109], v156, v155 op_sel_hi:[0,0,0]
	global_load_lds_dwordx4 v136, s[34:35]
	v_mfma_scale_f32_16x16x128_f8f6f4 v[94:97], v[2:9], v[208:215], v[94:97], v156, v155 op_sel_hi:[0,0,0]
	v_mfma_scale_f32_16x16x128_f8f6f4 v[90:93], v[18:25], v[208:215], v[90:93], v156, v155 op_sel_hi:[0,0,0]
	v_mfma_scale_f32_16x16x128_f8f6f4 v[78:81], v[2:9], v[216:223], v[78:81], v156, v155 op_sel_hi:[0,0,0]
	v_mfma_scale_f32_16x16x128_f8f6f4 v[74:77], v[18:25], v[216:223], v[74:77], v156, v155 op_sel_hi:[0,0,0]
	s_setprio 0
	s_setprio 1
	s_nop 0
	v_mfma_scale_f32_16x16x128_f8f6f4 v[118:121], v[164:171], v[192:199], v[118:121], v156, v155 op_sel_hi:[0,0,0]
	v_mfma_scale_f32_16x16x128_f8f6f4 v[114:117], v[172:179], v[192:199], v[114:117], v156, v155 op_sel_hi:[0,0,0]
	v_mfma_scale_f32_16x16x128_f8f6f4 v[102:105], v[164:171], v[200:207], v[102:105], v156, v155 op_sel_hi:[0,0,0]
	v_mfma_scale_f32_16x16x128_f8f6f4 v[98:101], v[172:179], v[200:207], v[98:101], v156, v155 op_sel_hi:[0,0,0]
	v_mfma_scale_f32_16x16x128_f8f6f4 v[86:89], v[164:171], v[208:215], v[86:89], v156, v155 op_sel_hi:[0,0,0]
	v_mfma_scale_f32_16x16x128_f8f6f4 v[82:85], v[172:179], v[208:215], v[82:85], v156, v155 op_sel_hi:[0,0,0]
	v_mfma_scale_f32_16x16x128_f8f6f4 v[70:73], v[164:171], v[216:223], v[70:73], v156, v155 op_sel_hi:[0,0,0]
	v_mfma_scale_f32_16x16x128_f8f6f4 v[66:69], v[172:179], v[216:223], v[66:69], v156, v155 op_sel_hi:[0,0,0]
	s_setprio 0
	s_barrier
	s_add_i32 s34, s64, s40
	s_mov_b32 m0, s34
	ds_read_b128 v[192:195], v154 offset:49152
	ds_read_b128 v[196:199], v154 offset:50176
	ds_read_b128 v[200:203], v154 offset:51200
	ds_read_b128 v[204:207], v154 offset:52224
	ds_read_b128 v[208:211], v154 offset:53248
	ds_read_b128 v[212:215], v154 offset:54272
	ds_read_b128 v[216:219], v154 offset:55296
	ds_read_b128 v[220:223], v154 offset:56320
	s_waitcnt vmcnt(2)
	s_waitcnt lgkmcnt(0)
	s_barrier
	s_setprio 1
	s_waitcnt lgkmcnt(0)
	s_nop 0
	v_mfma_scale_f32_16x16x128_f8f6f4 v[62:65], v[2:9], v[192:199], v[62:65], v156, v155 op_sel_hi:[0,0,0]
	global_load_lds_dwordx4 v132, s[90:91]
	s_add_i32 m0, s34, 0x2000
	v_mfma_scale_f32_16x16x128_f8f6f4 v[58:61], v[18:25], v[192:199], v[58:61], v156, v155 op_sel_hi:[0,0,0]
	s_add_u32 s30, s30, 0x40080
	s_addc_u32 s31, s31, 0
	v_mfma_scale_f32_16x16x128_f8f6f4 v[46:49], v[2:9], v[200:207], v[46:49], v156, v155 op_sel_hi:[0,0,0]
	s_add_i32 s34, s65, s40
	global_load_lds_dwordx4 v140, s[90:91]
	v_mfma_scale_f32_16x16x128_f8f6f4 v[42:45], v[18:25], v[200:207], v[42:45], v156, v155 op_sel_hi:[0,0,0]
	s_mov_b32 m0, s34
	s_nop 0
	v_mfma_scale_f32_16x16x128_f8f6f4 v[30:33], v[2:9], v[208:215], v[30:33], v156, v155 op_sel_hi:[0,0,0]
	global_load_lds_dwordx4 v132, s[30:31]
	s_add_i32 m0, s34, 0x2000
	v_mfma_scale_f32_16x16x128_f8f6f4 v[26:29], v[18:25], v[208:215], v[26:29], v156, v155 op_sel_hi:[0,0,0]
	s_nop 0
	global_load_lds_dwordx4 v140, s[30:31]
	v_mfma_scale_f32_16x16x128_f8f6f4 v[14:17], v[2:9], v[216:223], v[14:17], v156, v155 op_sel_hi:[0,0,0]
	s_mov_b32 m0, s50
	s_nop 0
	v_mfma_scale_f32_16x16x128_f8f6f4 v[10:13], v[18:25], v[216:223], v[10:13], v156, v155 op_sel_hi:[0,0,0]
	global_load_lds_dwordx4 v138, s[92:93]
	s_mov_b32 m0, s51
	s_setprio 0
	s_setprio 1
	s_nop 0
	v_mfma_scale_f32_16x16x128_f8f6f4 v[54:57], v[164:171], v[192:199], v[54:57], v156, v155 op_sel_hi:[0,0,0]
	s_nop 0
	global_load_lds_dwordx4 v136, s[92:93]
	v_mfma_scale_f32_16x16x128_f8f6f4 v[50:53], v[172:179], v[192:199], v[50:53], v156, v155 op_sel_hi:[0,0,0]
	v_mfma_scale_f32_16x16x128_f8f6f4 v[38:41], v[164:171], v[200:207], v[38:41], v156, v155 op_sel_hi:[0,0,0]
	v_mfma_scale_f32_16x16x128_f8f6f4 v[34:37], v[172:179], v[200:207], v[34:37], v156, v155 op_sel_hi:[0,0,0]
	v_mfma_scale_f32_16x16x128_f8f6f4 v[22:25], v[164:171], v[208:215], v[148:151], v156, v155 op_sel_hi:[0,0,0]
	v_mfma_scale_f32_16x16x128_f8f6f4 v[18:21], v[172:179], v[208:215], v[158:161], v156, v155 op_sel_hi:[0,0,0]
	v_mfma_scale_f32_16x16x128_f8f6f4 v[6:9], v[164:171], v[216:223], v[180:183], v156, v155 op_sel_hi:[0,0,0]
	v_mfma_scale_f32_16x16x128_f8f6f4 v[2:5], v[172:179], v[216:223], v[184:187], v156, v155 op_sel_hi:[0,0,0]
	s_setprio 0
	s_barrier
	s_add_i32 s63, s63, 2
	s_add_u32 s26, s26, 0x100
	s_addc_u32 s27, s27, 0
	s_add_u32 s61, s61, 0x100
	s_addc_u32 s62, s62, 0
	s_cmp_gt_u32 s63, 13
	s_cbranch_scc0 .LBB0_1084
	s_and_b64 vcc, exec, s[10:11]
	s_cbranch_vccz .LBB0_1087
	s_barrier

.LBB0_1159:
	ds_read_b128 v[166:169], v160
	ds_read_b128 v[170:173], v160 offset:1024
	ds_read_b128 v[174:177], v160 offset:2048
	ds_read_b128 v[178:181], v160 offset:3072
	ds_read_b128 v[182:185], v161
	ds_read_b128 v[186:189], v161 offset:1024
	ds_read_b128 v[224:227], v161 offset:2048
	ds_read_b128 v[228:231], v161 offset:3072
	s_add_u32 s38, s36, 0xfff20080
	s_addc_u32 s39, s37, -1
	s_cmp_eq_u32 s69, 52
	s_cselect_b32 s41, s31, s39
	s_cselect_b32 s40, s30, s38
	s_cselect_b32 s39, s35, s68
	s_cselect_b32 s38, s34, s1
	s_mov_b32 m0, s64
	ds_read_b128 v[192:195], v162
	ds_read_b128 v[196:199], v162 offset:1024
	ds_read_b128 v[200:203], v162 offset:2048
	ds_read_b128 v[204:207], v162 offset:3072
	ds_read_b128 v[208:211], v162 offset:4096
	ds_read_b128 v[212:215], v162 offset:5120
	ds_read_b128 v[216:219], v162 offset:6144
	ds_read_b128 v[220:223], v162 offset:7168
	s_waitcnt vmcnt(6)
	s_waitcnt lgkmcnt(0)
	s_barrier
	s_setprio 1
	s_waitcnt lgkmcnt(0)
	s_nop 0
	v_mfma_scale_f32_16x16x128_f8f6f4 v[126:129], v[166:173], v[192:199], v[126:129], v165, v164 op_sel_hi:[0,0,0]
	global_load_lds_dwordx4 v140, s[36:37]
	v_mfma_scale_f32_16x16x128_f8f6f4 v[122:125], v[174:181], v[192:199], v[122:125], v165, v164 op_sel_hi:[0,0,0]
	s_mov_b32 m0, s65
	v_mfma_scale_f32_16x16x128_f8f6f4 v[110:113], v[166:173], v[200:207], v[110:113], v165, v164 op_sel_hi:[0,0,0]
	s_nop 0
	v_mfma_scale_f32_16x16x128_f8f6f4 v[106:109], v[174:181], v[200:207], v[106:109], v165, v164 op_sel_hi:[0,0,0]
	global_load_lds_dwordx4 v142, s[36:37]
	v_mfma_scale_f32_16x16x128_f8f6f4 v[94:97], v[166:173], v[208:215], v[94:97], v165, v164 op_sel_hi:[0,0,0]
	v_mfma_scale_f32_16x16x128_f8f6f4 v[90:93], v[174:181], v[208:215], v[90:93], v165, v164 op_sel_hi:[0,0,0]
	v_mfma_scale_f32_16x16x128_f8f6f4 v[86:89], v[166:173], v[216:223], v[86:89], v165, v164 op_sel_hi:[0,0,0]
	v_mfma_scale_f32_16x16x128_f8f6f4 v[78:81], v[174:181], v[216:223], v[78:81], v165, v164 op_sel_hi:[0,0,0]
	s_setprio 0
	s_setprio 1
	s_nop 0
	v_mfma_scale_f32_16x16x128_f8f6f4 v[118:121], v[182:189], v[192:199], v[118:121], v165, v164 op_sel_hi:[0,0,0]
	v_mfma_scale_f32_16x16x128_f8f6f4 v[114:117], v[224:231], v[192:199], v[114:117], v165, v164 op_sel_hi:[0,0,0]
	v_mfma_scale_f32_16x16x128_f8f6f4 v[102:105], v[182:189], v[200:207], v[102:105], v165, v164 op_sel_hi:[0,0,0]
	v_mfma_scale_f32_16x16x128_f8f6f4 v[98:101], v[224:231], v[200:207], v[98:101], v165, v164 op_sel_hi:[0,0,0]
	v_mfma_scale_f32_16x16x128_f8f6f4 v[82:85], v[182:189], v[208:215], v[82:85], v165, v164 op_sel_hi:[0,0,0]
	v_mfma_scale_f32_16x16x128_f8f6f4 v[74:77], v[224:231], v[208:215], v[74:77], v165, v164 op_sel_hi:[0,0,0]
	v_mfma_scale_f32_16x16x128_f8f6f4 v[70:73], v[182:189], v[216:223], v[70:73], v165, v164 op_sel_hi:[0,0,0]
	v_mfma_scale_f32_16x16x128_f8f6f4 v[66:69], v[224:231], v[216:223], v[66:69], v165, v164 op_sel_hi:[0,0,0]
	s_setprio 0
	s_barrier
	s_add_i32 s70, s58, s50
	s_add_u32 s90, s38, s14
	s_addc_u32 s91, s39, s15
	s_mov_b32 m0, s70
	ds_read_b128 v[192:195], v162 offset:16384
	ds_read_b128 v[196:199], v162 offset:17408
	ds_read_b128 v[200:203], v162 offset:18432
	ds_read_b128 v[204:207], v162 offset:19456
	ds_read_b128 v[208:211], v162 offset:20480
	ds_read_b128 v[212:215], v162 offset:21504
	ds_read_b128 v[216:219], v162 offset:22528
	ds_read_b128 v[220:223], v162 offset:23552
	s_waitcnt vmcnt(2)
	s_waitcnt lgkmcnt(0)
	s_barrier
	s_setprio 1
	s_waitcnt lgkmcnt(0)
	s_nop 0
	v_mfma_scale_f32_16x16x128_f8f6f4 v[62:65], v[166:173], v[192:199], v[62:65], v165, v164 op_sel_hi:[0,0,0]
	global_load_lds_dwordx4 v130, s[38:39]
	s_add_i32 m0, s70, 0x2000
	v_mfma_scale_f32_16x16x128_f8f6f4 v[58:61], v[174:181], v[192:199], v[58:61], v165, v164 op_sel_hi:[0,0,0]
	s_add_u32 s70, s38, 0xe0000
	s_addc_u32 s71, s39, 0
	v_mfma_scale_f32_16x16x128_f8f6f4 v[46:49], v[166:173], v[200:207], v[46:49], v165, v164 op_sel_hi:[0,0,0]
	s_add_i32 s72, s59, s50
	global_load_lds_dwordx4 v138, s[38:39]
	v_mfma_scale_f32_16x16x128_f8f6f4 v[42:45], v[174:181], v[200:207], v[42:45], v165, v164 op_sel_hi:[0,0,0]
	s_mov_b32 m0, s72
	s_nop 0
	v_mfma_scale_f32_16x16x128_f8f6f4 v[30:33], v[166:173], v[208:215], v[30:33], v165, v164 op_sel_hi:[0,0,0]
	global_load_lds_dwordx4 v130, s[70:71]
	s_add_i32 m0, s72, 0x2000
	v_mfma_scale_f32_16x16x128_f8f6f4 v[26:29], v[174:181], v[208:215], v[26:29], v165, v164 op_sel_hi:[0,0,0]
	s_nop 0
	global_load_lds_dwordx4 v138, s[70:71]
	v_mfma_scale_f32_16x16x128_f8f6f4 v[14:17], v[166:173], v[216:223], v[14:17], v165, v164 op_sel_hi:[0,0,0]
	s_add_u32 s92, s40, s14
	s_addc_u32 s93, s41, s15
	v_mfma_scale_f32_16x16x128_f8f6f4 v[10:13], v[174:181], v[216:223], v[10:13], v165, v164 op_sel_hi:[0,0,0]
	s_mov_b32 m0, s51
	s_nop 0
	s_setprio 0
	s_setprio 1
	s_nop 0
	v_mfma_scale_f32_16x16x128_f8f6f4 v[54:57], v[182:189], v[192:199], v[54:57], v165, v164 op_sel_hi:[0,0,0]
	global_load_lds_dwordx4 v136, s[40:41]
	s_mov_b32 m0, s52
	v_mfma_scale_f32_16x16x128_f8f6f4 v[50:53], v[224:231], v[192:199], v[50:53], v165, v164 op_sel_hi:[0,0,0]
	s_nop 0
	global_load_lds_dwordx4 v132, s[40:41]
	v_mfma_scale_f32_16x16x128_f8f6f4 v[38:41], v[182:189], v[200:207], v[38:41], v165, v164 op_sel_hi:[0,0,0]
	v_mfma_scale_f32_16x16x128_f8f6f4 v[34:37], v[224:231], v[200:207], v[34:37], v165, v164 op_sel_hi:[0,0,0]
	v_mfma_scale_f32_16x16x128_f8f6f4 v[232:235], v[182:189], v[208:215], v[22:25], v165, v164 op_sel_hi:[0,0,0]
	v_mfma_scale_f32_16x16x128_f8f6f4 v[236:239], v[224:231], v[208:215], v[18:21], v165, v164 op_sel_hi:[0,0,0]
	v_mfma_scale_f32_16x16x128_f8f6f4 v[182:185], v[182:189], v[216:223], v[6:9], v165, v164 op_sel_hi:[0,0,0]
	v_mfma_scale_f32_16x16x128_f8f6f4 v[186:189], v[224:231], v[216:223], v[2:5], v165, v164 op_sel_hi:[0,0,0]
	s_setprio 0
	s_barrier
	s_add_i32 s70, 0, 0x18000
	s_add_i32 s71, 0, 0x1c000
	v_add_u32_e32 v22, s70, v158
	v_add_u32_e32 v178, s71, v158
	s_nop 0
	ds_read_b128 v[2:5], v22
	ds_read_b128 v[6:9], v22 offset:1024
	ds_read_b128 v[18:21], v22 offset:2048
	ds_read_b128 v[22:25], v22 offset:3072
	ds_read_b128 v[166:169], v178
	ds_read_b128 v[170:173], v178 offset:1024
	ds_read_b128 v[174:177], v178 offset:2048
	ds_read_b128 v[178:181], v178 offset:3072
	s_add_u32 s40, s40, 0xe0000
	s_addc_u32 s41, s41, 0
	s_mov_b32 m0, s53
	ds_read_b128 v[192:195], v162 offset:32768
	ds_read_b128 v[196:199], v162 offset:33792
	ds_read_b128 v[200:203], v162 offset:34816
	ds_read_b128 v[204:207], v162 offset:35840
	ds_read_b128 v[208:211], v162 offset:36864
	ds_read_b128 v[212:215], v162 offset:37888
	ds_read_b128 v[216:219], v162 offset:38912
	ds_read_b128 v[220:223], v162 offset:39936
	s_waitcnt vmcnt(6)
	s_waitcnt lgkmcnt(0)
	s_barrier
	s_setprio 1
	s_waitcnt lgkmcnt(0)
	s_nop 0
	v_mfma_scale_f32_16x16x128_f8f6f4 v[126:129], v[2:9], v[192:199], v[126:129], v165, v164 op_sel_hi:[0,0,0]
	global_load_lds_dwordx4 v136, s[40:41]
	v_mfma_scale_f32_16x16x128_f8f6f4 v[122:125], v[18:25], v[192:199], v[122:125], v165, v164 op_sel_hi:[0,0,0]
	s_mov_b32 m0, s54
	v_mfma_scale_f32_16x16x128_f8f6f4 v[110:113], v[2:9], v[200:207], v[110:113], v165, v164 op_sel_hi:[0,0,0]
	s_nop 0
	v_mfma_scale_f32_16x16x128_f8f6f4 v[106:109], v[18:25], v[200:207], v[106:109], v165, v164 op_sel_hi:[0,0,0]
	global_load_lds_dwordx4 v132, s[40:41]
	v_mfma_scale_f32_16x16x128_f8f6f4 v[94:97], v[2:9], v[208:215], v[94:97], v165, v164 op_sel_hi:[0,0,0]
	v_mfma_scale_f32_16x16x128_f8f6f4 v[90:93], v[18:25], v[208:215], v[90:93], v165, v164 op_sel_hi:[0,0,0]
	v_mfma_scale_f32_16x16x128_f8f6f4 v[86:89], v[2:9], v[216:223], v[86:89], v165, v164 op_sel_hi:[0,0,0]
	v_mfma_scale_f32_16x16x128_f8f6f4 v[78:81], v[18:25], v[216:223], v[78:81], v165, v164 op_sel_hi:[0,0,0]
	s_setprio 0
	s_setprio 1
	s_nop 0
	v_mfma_scale_f32_16x16x128_f8f6f4 v[118:121], v[166:173], v[192:199], v[118:121], v165, v164 op_sel_hi:[0,0,0]
	v_mfma_scale_f32_16x16x128_f8f6f4 v[114:117], v[174:181], v[192:199], v[114:117], v165, v164 op_sel_hi:[0,0,0]
	v_mfma_scale_f32_16x16x128_f8f6f4 v[102:105], v[166:173], v[200:207], v[102:105], v165, v164 op_sel_hi:[0,0,0]
	v_mfma_scale_f32_16x16x128_f8f6f4 v[98:101], v[174:181], v[200:207], v[98:101], v165, v164 op_sel_hi:[0,0,0]
	v_mfma_scale_f32_16x16x128_f8f6f4 v[82:85], v[166:173], v[208:215], v[82:85], v165, v164 op_sel_hi:[0,0,0]
	v_mfma_scale_f32_16x16x128_f8f6f4 v[74:77], v[174:181], v[208:215], v[74:77], v165, v164 op_sel_hi:[0,0,0]
	v_mfma_scale_f32_16x16x128_f8f6f4 v[70:73], v[166:173], v[216:223], v[70:73], v165, v164 op_sel_hi:[0,0,0]
	v_mfma_scale_f32_16x16x128_f8f6f4 v[66:69], v[174:181], v[216:223], v[66:69], v165, v164 op_sel_hi:[0,0,0]
	s_setprio 0
	s_barrier
	s_add_i32 s40, s70, s50
	s_mov_b32 m0, s40
	ds_read_b128 v[192:195], v162 offset:49152
	ds_read_b128 v[196:199], v162 offset:50176
	ds_read_b128 v[200:203], v162 offset:51200
	ds_read_b128 v[204:207], v162 offset:52224
	ds_read_b128 v[208:211], v162 offset:53248
	ds_read_b128 v[212:215], v162 offset:54272
	ds_read_b128 v[216:219], v162 offset:55296
	ds_read_b128 v[220:223], v162 offset:56320
	s_waitcnt vmcnt(2)
	s_waitcnt lgkmcnt(0)
	s_barrier
	s_setprio 1
	s_waitcnt lgkmcnt(0)
	s_nop 0
	v_mfma_scale_f32_16x16x128_f8f6f4 v[62:65], v[2:9], v[192:199], v[62:65], v165, v164 op_sel_hi:[0,0,0]
	global_load_lds_dwordx4 v130, s[90:91]
	s_add_i32 m0, s40, 0x2000
	v_mfma_scale_f32_16x16x128_f8f6f4 v[58:61], v[18:25], v[192:199], v[58:61], v165, v164 op_sel_hi:[0,0,0]
	s_add_u32 s38, s38, 0xe0080
	s_addc_u32 s39, s39, 0
	v_mfma_scale_f32_16x16x128_f8f6f4 v[46:49], v[2:9], v[200:207], v[46:49], v165, v164 op_sel_hi:[0,0,0]
	s_add_i32 s40, s71, s50
	global_load_lds_dwordx4 v138, s[90:91]
	v_mfma_scale_f32_16x16x128_f8f6f4 v[42:45], v[18:25], v[200:207], v[42:45], v165, v164 op_sel_hi:[0,0,0]
	s_mov_b32 m0, s40
	s_nop 0
	v_mfma_scale_f32_16x16x128_f8f6f4 v[30:33], v[2:9], v[208:215], v[30:33], v165, v164 op_sel_hi:[0,0,0]
	global_load_lds_dwordx4 v130, s[38:39]
	s_add_i32 m0, s40, 0x2000
	v_mfma_scale_f32_16x16x128_f8f6f4 v[26:29], v[18:25], v[208:215], v[26:29], v165, v164 op_sel_hi:[0,0,0]
	s_nop 0
	global_load_lds_dwordx4 v138, s[38:39]
	v_mfma_scale_f32_16x16x128_f8f6f4 v[14:17], v[2:9], v[216:223], v[14:17], v165, v164 op_sel_hi:[0,0,0]
	s_mov_b32 m0, s56
	s_nop 0
	v_mfma_scale_f32_16x16x128_f8f6f4 v[10:13], v[18:25], v[216:223], v[10:13], v165, v164 op_sel_hi:[0,0,0]
	global_load_lds_dwordx4 v136, s[92:93]
	s_mov_b32 m0, s57
	s_setprio 0
	s_setprio 1
	s_nop 0
	v_mfma_scale_f32_16x16x128_f8f6f4 v[54:57], v[166:173], v[192:199], v[54:57], v165, v164 op_sel_hi:[0,0,0]
	s_nop 0
	global_load_lds_dwordx4 v132, s[92:93]
	v_mfma_scale_f32_16x16x128_f8f6f4 v[50:53], v[174:181], v[192:199], v[50:53], v165, v164 op_sel_hi:[0,0,0]
	v_mfma_scale_f32_16x16x128_f8f6f4 v[38:41], v[166:173], v[200:207], v[38:41], v165, v164 op_sel_hi:[0,0,0]
	v_mfma_scale_f32_16x16x128_f8f6f4 v[34:37], v[174:181], v[200:207], v[34:37], v165, v164 op_sel_hi:[0,0,0]
	v_mfma_scale_f32_16x16x128_f8f6f4 v[22:25], v[166:173], v[208:215], v[232:235], v165, v164 op_sel_hi:[0,0,0]
	v_mfma_scale_f32_16x16x128_f8f6f4 v[18:21], v[174:181], v[208:215], v[236:239], v165, v164 op_sel_hi:[0,0,0]
	v_mfma_scale_f32_16x16x128_f8f6f4 v[6:9], v[166:173], v[216:223], v[182:185], v165, v164 op_sel_hi:[0,0,0]
	v_mfma_scale_f32_16x16x128_f8f6f4 v[2:5], v[174:181], v[216:223], v[186:189], v165, v164 op_sel_hi:[0,0,0]
	s_setprio 0
	s_barrier
	s_add_i32 s69, s69, 2
	s_add_u32 s36, s36, 0x100
	s_addc_u32 s37, s37, 0
	s_add_u32 s1, s1, 0x100
	s_addc_u32 s68, s68, 0
	s_cmp_gt_u32 s69, 53
	s_cbranch_scc0 .LBB0_1159
	s_and_b64 vcc, exec, s[16:17]
	s_cbranch_vccz .LBB0_1162
	s_barrier

.LBB0_1180:
	ds_read_b128 v[158:161], v152
	ds_read_b128 v[162:165], v152 offset:1024
	ds_read_b128 v[166:169], v152 offset:2048
	ds_read_b128 v[170:173], v152 offset:3072
	ds_read_b128 v[174:177], v153
	ds_read_b128 v[178:181], v153 offset:1024
	ds_read_b128 v[182:185], v153 offset:2048
	ds_read_b128 v[186:189], v153 offset:3072
	s_add_i32 s70, s24, 2
	s_add_u32 s25, s22, 0xfff20080
	s_addc_u32 s26, s23, -1
	s_cmp_eq_u32 s58, s24
	s_cselect_b32 s24, s18, s68
	s_cselect_b32 s27, s17, s26
	s_cselect_b32 s26, s16, s25
	s_cselect_b32 s25, s19, s69
	s_add_i32 m0, s21, 0xc000
	ds_read_b128 v[192:195], v154
	ds_read_b128 v[196:199], v154 offset:1024
	ds_read_b128 v[200:203], v154 offset:2048
	ds_read_b128 v[204:207], v154 offset:3072
	ds_read_b128 v[208:211], v154 offset:4096
	ds_read_b128 v[212:215], v154 offset:5120
	ds_read_b128 v[216:219], v154 offset:6144
	ds_read_b128 v[220:223], v154 offset:7168
	s_waitcnt vmcnt(6)
	s_waitcnt lgkmcnt(0)
	s_barrier
	s_setprio 1
	s_waitcnt lgkmcnt(0)
	s_nop 0
	v_mfma_scale_f32_16x16x128_f8f6f4 v[120:123], v[158:165], v[192:199], v[120:123], v156, v155 op_sel_hi:[0,0,0]
	global_load_lds_dwordx4 v136, s[22:23]
	v_mfma_scale_f32_16x16x128_f8f6f4 v[124:127], v[166:173], v[192:199], v[124:127], v156, v155 op_sel_hi:[0,0,0]
	s_add_i32 m0, s21, 0xe000
	v_mfma_scale_f32_16x16x128_f8f6f4 v[108:111], v[158:165], v[200:207], v[108:111], v156, v155 op_sel_hi:[0,0,0]
	s_nop 0
	v_mfma_scale_f32_16x16x128_f8f6f4 v[104:107], v[166:173], v[200:207], v[104:107], v156, v155 op_sel_hi:[0,0,0]
	global_load_lds_dwordx4 v138, s[22:23]
	v_mfma_scale_f32_16x16x128_f8f6f4 v[92:95], v[158:165], v[208:215], v[92:95], v156, v155 op_sel_hi:[0,0,0]
	v_mfma_scale_f32_16x16x128_f8f6f4 v[88:91], v[166:173], v[208:215], v[88:91], v156, v155 op_sel_hi:[0,0,0]
	v_mfma_scale_f32_16x16x128_f8f6f4 v[76:79], v[158:165], v[216:223], v[76:79], v156, v155 op_sel_hi:[0,0,0]
	v_mfma_scale_f32_16x16x128_f8f6f4 v[72:75], v[166:173], v[216:223], v[72:75], v156, v155 op_sel_hi:[0,0,0]
	s_setprio 0
	s_setprio 1
	s_nop 0
	v_mfma_scale_f32_16x16x128_f8f6f4 v[116:119], v[174:181], v[192:199], v[116:119], v156, v155 op_sel_hi:[0,0,0]
	v_mfma_scale_f32_16x16x128_f8f6f4 v[112:115], v[182:189], v[192:199], v[112:115], v156, v155 op_sel_hi:[0,0,0]
	v_mfma_scale_f32_16x16x128_f8f6f4 v[100:103], v[174:181], v[200:207], v[100:103], v156, v155 op_sel_hi:[0,0,0]
	v_mfma_scale_f32_16x16x128_f8f6f4 v[96:99], v[182:189], v[200:207], v[96:99], v156, v155 op_sel_hi:[0,0,0]
	v_mfma_scale_f32_16x16x128_f8f6f4 v[84:87], v[174:181], v[208:215], v[84:87], v156, v155 op_sel_hi:[0,0,0]
	v_mfma_scale_f32_16x16x128_f8f6f4 v[80:83], v[182:189], v[208:215], v[80:83], v156, v155 op_sel_hi:[0,0,0]
	v_mfma_scale_f32_16x16x128_f8f6f4 v[68:71], v[174:181], v[216:223], v[68:71], v156, v155 op_sel_hi:[0,0,0]
	v_mfma_scale_f32_16x16x128_f8f6f4 v[64:67], v[182:189], v[216:223], v[64:67], v156, v155 op_sel_hi:[0,0,0]
	s_setprio 0
	s_barrier
	s_add_i32 s71, s62, s38
	s_add_u32 s90, s24, s8
	s_addc_u32 s91, s25, s9
	s_mov_b32 m0, s71
	ds_read_b128 v[192:195], v154 offset:16384
	ds_read_b128 v[196:199], v154 offset:17408
	ds_read_b128 v[200:203], v154 offset:18432
	ds_read_b128 v[204:207], v154 offset:19456
	ds_read_b128 v[208:211], v154 offset:20480
	ds_read_b128 v[212:215], v154 offset:21504
	ds_read_b128 v[216:219], v154 offset:22528
	ds_read_b128 v[220:223], v154 offset:23552
	s_waitcnt vmcnt(2)
	s_waitcnt lgkmcnt(0)
	s_barrier
	s_setprio 1
	s_waitcnt lgkmcnt(0)
	s_nop 0
	v_mfma_scale_f32_16x16x128_f8f6f4 v[60:63], v[158:165], v[192:199], v[60:63], v156, v155 op_sel_hi:[0,0,0]
	global_load_lds_dwordx4 v128, s[24:25]
	s_add_i32 m0, s71, 0x2000
	v_mfma_scale_f32_16x16x128_f8f6f4 v[56:59], v[166:173], v[192:199], v[56:59], v156, v155 op_sel_hi:[0,0,0]
	s_add_u32 s72, s24, 0xe0000
	s_addc_u32 s73, s25, 0
	v_mfma_scale_f32_16x16x128_f8f6f4 v[44:47], v[158:165], v[200:207], v[44:47], v156, v155 op_sel_hi:[0,0,0]
	s_add_i32 s71, s63, s38
	global_load_lds_dwordx4 v134, s[24:25]
	v_mfma_scale_f32_16x16x128_f8f6f4 v[40:43], v[166:173], v[200:207], v[40:43], v156, v155 op_sel_hi:[0,0,0]
	s_mov_b32 m0, s71
	s_add_u32 s92, s26, s8
	v_mfma_scale_f32_16x16x128_f8f6f4 v[28:31], v[158:165], v[208:215], v[28:31], v156, v155 op_sel_hi:[0,0,0]
	s_addc_u32 s93, s27, s9
	s_nop 0
	v_mfma_scale_f32_16x16x128_f8f6f4 v[24:27], v[166:173], v[208:215], v[24:27], v156, v155 op_sel_hi:[0,0,0]
	global_load_lds_dwordx4 v128, s[72:73]
	s_add_i32 m0, s71, 0x2000
	v_mfma_scale_f32_16x16x128_f8f6f4 v[12:15], v[158:165], v[216:223], v[12:15], v156, v155 op_sel_hi:[0,0,0]
	s_nop 0
	global_load_lds_dwordx4 v134, s[72:73]
	v_mfma_scale_f32_16x16x128_f8f6f4 v[8:11], v[166:173], v[216:223], v[8:11], v156, v155 op_sel_hi:[0,0,0]
	s_mov_b32 m0, s21
	s_nop 0
	s_setprio 0
	s_setprio 1
	s_nop 0
	v_mfma_scale_f32_16x16x128_f8f6f4 v[52:55], v[174:181], v[192:199], v[52:55], v156, v155 op_sel_hi:[0,0,0]
	global_load_lds_dwordx4 v132, s[26:27]
	s_mov_b32 m0, s39
	v_mfma_scale_f32_16x16x128_f8f6f4 v[48:51], v[182:189], v[192:199], v[48:51], v156, v155 op_sel_hi:[0,0,0]
	s_nop 0
	global_load_lds_dwordx4 v130, s[26:27]
	v_mfma_scale_f32_16x16x128_f8f6f4 v[36:39], v[174:181], v[200:207], v[36:39], v156, v155 op_sel_hi:[0,0,0]
	v_mfma_scale_f32_16x16x128_f8f6f4 v[32:35], v[182:189], v[200:207], v[32:35], v156, v155 op_sel_hi:[0,0,0]
	v_mfma_scale_f32_16x16x128_f8f6f4 v[140:143], v[174:181], v[208:215], v[20:23], v156, v155 op_sel_hi:[0,0,0]
	v_mfma_scale_f32_16x16x128_f8f6f4 v[224:227], v[182:189], v[208:215], v[16:19], v156, v155 op_sel_hi:[0,0,0]
	v_mfma_scale_f32_16x16x128_f8f6f4 v[174:177], v[174:181], v[216:223], v[4:7], v156, v155 op_sel_hi:[0,0,0]
	v_mfma_scale_f32_16x16x128_f8f6f4 v[178:181], v[182:189], v[216:223], v[0:3], v156, v155 op_sel_hi:[0,0,0]
	s_setprio 0
	s_barrier
	s_add_i32 s71, 0, 0x18000
	s_add_i32 s72, 0, 0x1c000
	v_add_u32_e32 v20, s71, v150
	v_add_u32_e32 v157, s72, v150
	s_nop 0
	ds_read_b128 v[0:3], v20
	ds_read_b128 v[4:7], v20 offset:1024
	ds_read_b128 v[16:19], v20 offset:2048
	ds_read_b128 v[20:23], v20 offset:3072
	ds_read_b128 v[158:161], v157
	ds_read_b128 v[162:165], v157 offset:1024
	ds_read_b128 v[166:169], v157 offset:2048
	ds_read_b128 v[170:173], v157 offset:3072
	s_add_u32 s26, s26, 0xe0000
	s_addc_u32 s27, s27, 0
	s_mov_b32 m0, s40
	ds_read_b128 v[192:195], v154 offset:32768
	ds_read_b128 v[196:199], v154 offset:33792
	ds_read_b128 v[200:203], v154 offset:34816
	ds_read_b128 v[204:207], v154 offset:35840
	ds_read_b128 v[208:211], v154 offset:36864
	ds_read_b128 v[212:215], v154 offset:37888
	ds_read_b128 v[216:219], v154 offset:38912
	ds_read_b128 v[220:223], v154 offset:39936
	s_waitcnt vmcnt(6)
	s_waitcnt lgkmcnt(0)
	s_barrier
	s_setprio 1
	s_waitcnt lgkmcnt(0)
	s_nop 0
	v_mfma_scale_f32_16x16x128_f8f6f4 v[120:123], v[0:7], v[192:199], v[120:123], v156, v155 op_sel_hi:[0,0,0]
	global_load_lds_dwordx4 v132, s[26:27]
	v_mfma_scale_f32_16x16x128_f8f6f4 v[124:127], v[16:23], v[192:199], v[124:127], v156, v155 op_sel_hi:[0,0,0]
	s_mov_b32 m0, s41
	v_mfma_scale_f32_16x16x128_f8f6f4 v[108:111], v[0:7], v[200:207], v[108:111], v156, v155 op_sel_hi:[0,0,0]
	s_nop 0
	v_mfma_scale_f32_16x16x128_f8f6f4 v[104:107], v[16:23], v[200:207], v[104:107], v156, v155 op_sel_hi:[0,0,0]
	global_load_lds_dwordx4 v130, s[26:27]
	v_mfma_scale_f32_16x16x128_f8f6f4 v[92:95], v[0:7], v[208:215], v[92:95], v156, v155 op_sel_hi:[0,0,0]
	v_mfma_scale_f32_16x16x128_f8f6f4 v[88:91], v[16:23], v[208:215], v[88:91], v156, v155 op_sel_hi:[0,0,0]
	v_mfma_scale_f32_16x16x128_f8f6f4 v[76:79], v[0:7], v[216:223], v[76:79], v156, v155 op_sel_hi:[0,0,0]
	v_mfma_scale_f32_16x16x128_f8f6f4 v[72:75], v[16:23], v[216:223], v[72:75], v156, v155 op_sel_hi:[0,0,0]
	s_setprio 0
	s_setprio 1
	s_nop 0
	v_mfma_scale_f32_16x16x128_f8f6f4 v[116:119], v[158:165], v[192:199], v[116:119], v156, v155 op_sel_hi:[0,0,0]
	v_mfma_scale_f32_16x16x128_f8f6f4 v[112:115], v[166:173], v[192:199], v[112:115], v156, v155 op_sel_hi:[0,0,0]
	v_mfma_scale_f32_16x16x128_f8f6f4 v[100:103], v[158:165], v[200:207], v[100:103], v156, v155 op_sel_hi:[0,0,0]
	v_mfma_scale_f32_16x16x128_f8f6f4 v[96:99], v[166:173], v[200:207], v[96:99], v156, v155 op_sel_hi:[0,0,0]
	v_mfma_scale_f32_16x16x128_f8f6f4 v[84:87], v[158:165], v[208:215], v[84:87], v156, v155 op_sel_hi:[0,0,0]
	v_mfma_scale_f32_16x16x128_f8f6f4 v[80:83], v[166:173], v[208:215], v[80:83], v156, v155 op_sel_hi:[0,0,0]
	v_mfma_scale_f32_16x16x128_f8f6f4 v[68:71], v[158:165], v[216:223], v[68:71], v156, v155 op_sel_hi:[0,0,0]
	v_mfma_scale_f32_16x16x128_f8f6f4 v[64:67], v[166:173], v[216:223], v[64:67], v156, v155 op_sel_hi:[0,0,0]
	s_setprio 0
	s_barrier
	s_add_i32 s26, s71, s38
	s_mov_b32 m0, s26
	ds_read_b128 v[192:195], v154 offset:49152
	ds_read_b128 v[196:199], v154 offset:50176
	ds_read_b128 v[200:203], v154 offset:51200
	ds_read_b128 v[204:207], v154 offset:52224
	ds_read_b128 v[208:211], v154 offset:53248
	ds_read_b128 v[212:215], v154 offset:54272
	ds_read_b128 v[216:219], v154 offset:55296
	ds_read_b128 v[220:223], v154 offset:56320
	s_waitcnt vmcnt(2)
	s_waitcnt lgkmcnt(0)
	s_barrier
	s_setprio 1
	s_waitcnt lgkmcnt(0)
	s_nop 0
	v_mfma_scale_f32_16x16x128_f8f6f4 v[60:63], v[0:7], v[192:199], v[60:63], v156, v155 op_sel_hi:[0,0,0]
	global_load_lds_dwordx4 v128, s[90:91]
	s_add_i32 m0, s26, 0x2000
	v_mfma_scale_f32_16x16x128_f8f6f4 v[56:59], v[16:23], v[192:199], v[56:59], v156, v155 op_sel_hi:[0,0,0]
	s_add_u32 s24, s24, 0xe0080
	s_addc_u32 s25, s25, 0
	v_mfma_scale_f32_16x16x128_f8f6f4 v[44:47], v[0:7], v[200:207], v[44:47], v156, v155 op_sel_hi:[0,0,0]
	s_add_i32 s26, s72, s38
	global_load_lds_dwordx4 v134, s[90:91]
	v_mfma_scale_f32_16x16x128_f8f6f4 v[40:43], v[16:23], v[200:207], v[40:43], v156, v155 op_sel_hi:[0,0,0]
	s_mov_b32 m0, s26
	s_nop 0
	v_mfma_scale_f32_16x16x128_f8f6f4 v[28:31], v[0:7], v[208:215], v[28:31], v156, v155 op_sel_hi:[0,0,0]
	global_load_lds_dwordx4 v128, s[24:25]
	s_add_i32 m0, s26, 0x2000
	v_mfma_scale_f32_16x16x128_f8f6f4 v[24:27], v[16:23], v[208:215], v[24:27], v156, v155 op_sel_hi:[0,0,0]
	s_nop 0
	global_load_lds_dwordx4 v134, s[24:25]
	v_mfma_scale_f32_16x16x128_f8f6f4 v[12:15], v[0:7], v[216:223], v[12:15], v156, v155 op_sel_hi:[0,0,0]
	s_mov_b32 m0, s55
	s_nop 0
	v_mfma_scale_f32_16x16x128_f8f6f4 v[8:11], v[16:23], v[216:223], v[8:11], v156, v155 op_sel_hi:[0,0,0]
	global_load_lds_dwordx4 v132, s[92:93]
	s_mov_b32 m0, s56
	s_setprio 0
	s_setprio 1
	s_nop 0
	v_mfma_scale_f32_16x16x128_f8f6f4 v[52:55], v[158:165], v[192:199], v[52:55], v156, v155 op_sel_hi:[0,0,0]
	s_nop 0
	global_load_lds_dwordx4 v130, s[92:93]
	v_mfma_scale_f32_16x16x128_f8f6f4 v[48:51], v[166:173], v[192:199], v[48:51], v156, v155 op_sel_hi:[0,0,0]
	v_mfma_scale_f32_16x16x128_f8f6f4 v[36:39], v[158:165], v[200:207], v[36:39], v156, v155 op_sel_hi:[0,0,0]
	v_mfma_scale_f32_16x16x128_f8f6f4 v[32:35], v[166:173], v[200:207], v[32:35], v156, v155 op_sel_hi:[0,0,0]
	v_mfma_scale_f32_16x16x128_f8f6f4 v[20:23], v[158:165], v[208:215], v[140:143], v156, v155 op_sel_hi:[0,0,0]
	v_mfma_scale_f32_16x16x128_f8f6f4 v[16:19], v[166:173], v[208:215], v[224:227], v156, v155 op_sel_hi:[0,0,0]
	v_mfma_scale_f32_16x16x128_f8f6f4 v[4:7], v[158:165], v[216:223], v[174:177], v156, v155 op_sel_hi:[0,0,0]
	v_mfma_scale_f32_16x16x128_f8f6f4 v[0:3], v[166:173], v[216:223], v[178:181], v156, v155 op_sel_hi:[0,0,0]
	s_setprio 0
	s_barrier
	s_add_u32 s22, s22, 0x100
	s_addc_u32 s23, s23, 0
	s_add_u32 s68, s68, 0x100
	s_addc_u32 s69, s69, 0
	s_cmp_ge_i32 s70, s54
	s_mov_b32 s24, s70
	s_cbranch_scc0 .LBB0_1180
